# gate path log-sigmoid via v_log_f32 (all original pads kept) + GEMM K-loops staging loads in scalar-base form
# speedup vs baseline: 1.0171x; 1.0171x over previous
.LBB0_146:
	s_or_b64 exec, exec, s[72:73]
	v_lshl_add_u64 v[70:71], v[78:79], 0, s[66:67]
	s_waitcnt lgkmcnt(0)
	v_mfma_f32_16x16x32_bf16 v[78:81], v[6:9], v[66:69], 0
	s_add_i32 s70, s96, s70
	s_cmpk_lt_i32 s70, 0x100
	v_lshl_add_u64 v[76:77], v[76:77], 0, s[24:25]
	s_nop 4
	v_add_f32_e32 v78, v10, v78
	v_mul_f32_e64 v82, |v78|, s35
	v_exp_f32_e32 v89, v82
	v_add_f32_e32 v83, v11, v79
	v_min_f32_e32 v82, 0, v78
	v_mul_f32_e64 v78, |v83|, s35
	v_exp_f32_e32 v116, v78
	v_add_f32_e32 v80, v12, v80
	v_min_f32_e32 v83, 0, v83
	v_add_f32_e32 v81, v13, v81
	s_nop 0
	s_nop 0
	s_nop 0
	s_nop 0
	s_nop 0
	s_nop 0
	s_nop 0
	s_nop 0
	s_nop 0
	s_nop 0
	s_nop 0
	s_nop 0
	s_nop 0
	s_nop 0
	s_nop 0
	s_nop 0
	s_nop 0
	v_mul_f32_e64 v92, |v80|, s35
	v_exp_f32_e32 v118, v92
	v_min_f32_e32 v80, 0, v80
	s_nop 0
	s_nop 1
	s_nop 1
	s_nop 1
	s_nop 1
	s_nop 1
	s_nop 1
	v_add_f32_e32 v91, 1.0, v116
	v_log_f32_e32 v91, v91
	s_nop 1
	v_mul_f32_e32 v91, 0x3f317218, v91
	s_nop 1
	s_nop 1
	s_nop 1
	v_add_f32_e32 v90, 1.0, v89
	v_log_f32_e32 v90, v90
	s_nop 1
	v_mul_f32_e32 v90, 0x3f317218, v90
	s_nop 1
	v_pk_add_f32 v[90:91], v[82:83], v[90:91] neg_lo:[0,1] neg_hi:[0,1]
	v_mul_f32_e64 v82, |v81|, s35
	v_exp_f32_e32 v119, v82
	v_min_f32_e32 v81, 0, v81
	s_nop 0
	s_nop 0
	s_nop 0
	s_nop 0
	s_nop 0
	s_nop 0
	s_nop 0
	s_nop 0
	s_nop 0
	s_nop 0
	s_nop 0
	s_nop 0
	s_nop 0
	s_nop 0
	s_nop 0
	s_nop 0
	s_nop 0
	s_nop 0
	s_nop 0
	v_lshl_add_u64 v[94:95], s[2:3], 2, v[70:71]
	s_nop 0
	s_nop 1
	s_nop 1
	s_nop 1
	s_nop 1
	s_nop 1
	s_nop 1
	s_nop 1
	v_add_f32_e32 v83, 1.0, v119
	v_log_f32_e32 v83, v83
	s_nop 1
	v_mul_f32_e32 v83, 0x3f317218, v83
	s_nop 1
	s_nop 1
	s_nop 1
	v_add_f32_e32 v82, 1.0, v118
	v_log_f32_e32 v82, v82
	s_nop 1
	v_mul_f32_e32 v82, 0x3f317218, v82
	s_nop 1
	v_pk_add_f32 v[80:81], v[80:81], v[82:83] neg_lo:[0,1] neg_hi:[0,1]
	s_nop 0
	v_pk_mul_f32 v[82:83], v[80:81], s[44:45] op_sel_hi:[1,0]
	v_pk_mul_f32 v[80:81], v[90:91], s[44:45] op_sel_hi:[1,0]
	v_mfma_f32_16x16x32_bf16 v[90:93], v[2:5], v[66:69], 0
	global_store_dwordx4 v[94:95], v[80:83], off
	s_nop 6
	v_add_f32_e32 v89, v14, v90
	v_mul_f32_e64 v90, |v89|, s35
	v_exp_f32_e32 v118, v90
	v_min_f32_e32 v80, 0, v89
	v_add_f32_e32 v81, v15, v91
	v_mul_f32_e64 v82, |v81|, s35
	v_exp_f32_e32 v119, v82
	v_min_f32_e32 v81, 0, v81
	s_nop 0
	s_nop 0
	v_add_f32_e32 v89, v16, v92
	s_nop 0
	s_nop 0
	s_nop 0
	s_nop 0
	s_nop 0
	s_nop 0
	s_nop 0
	s_nop 0
	s_nop 0
	s_nop 0
	s_nop 0
	s_nop 0
	s_nop 0
	s_nop 0
	s_nop 0
	s_nop 0
	s_nop 0
	v_mul_f32_e64 v90, |v89|, s35
	s_nop 1
	s_nop 1
	s_nop 1
	s_nop 1
	s_nop 1
	s_nop 1
	s_nop 1
	v_add_f32_e32 v83, 1.0, v119
	v_log_f32_e32 v83, v83
	s_nop 1
	v_mul_f32_e32 v83, 0x3f317218, v83
	s_nop 1
	v_exp_f32_e32 v119, v90
	s_nop 1
	s_nop 1
	v_add_f32_e32 v82, 1.0, v118
	v_log_f32_e32 v82, v82
	s_nop 1
	v_mul_f32_e32 v82, 0x3f317218, v82
	s_nop 1
	v_pk_add_f32 v[80:81], v[80:81], v[82:83] neg_lo:[0,1] neg_hi:[0,1]
	v_min_f32_e32 v82, 0, v89
	v_add_f32_e32 v83, v17, v93
	v_mul_f32_e64 v90, |v83|, s35
	v_exp_f32_e32 v118, v90
	v_min_f32_e32 v83, 0, v83
	v_pk_mul_f32 v[80:81], v[80:81], s[44:45] op_sel_hi:[1,0]
	s_nop 0
	s_nop 0
	s_nop 0
	s_nop 0
	s_nop 0
	s_nop 0
	s_nop 0
	s_nop 0
	s_nop 0
	s_nop 0
	s_nop 0
	s_nop 0
	s_nop 0
	s_nop 0
	s_nop 0
	s_nop 0
	s_nop 0
	s_nop 0
	v_lshl_add_u64 v[94:95], s[10:11], 2, v[70:71]
	s_nop 0
	s_nop 1
	s_nop 1
	s_nop 1
	s_nop 1
	s_nop 1
	s_nop 1
	s_nop 1
	v_add_f32_e32 v91, 1.0, v118
	v_log_f32_e32 v91, v91
	s_nop 1
	v_mul_f32_e32 v91, 0x3f317218, v91
	s_nop 1
	s_nop 1
	s_nop 1
	v_add_f32_e32 v90, 1.0, v119
	v_log_f32_e32 v90, v90
	s_nop 1
	v_mul_f32_e32 v90, 0x3f317218, v90
	s_nop 1
	v_pk_add_f32 v[82:83], v[82:83], v[90:91] neg_lo:[0,1] neg_hi:[0,1]
	v_mfma_f32_16x16x32_bf16 v[90:93], v[22:25], v[66:69], 0
	v_mul_f32_e64 v82, v82, s44
	v_mul_f32_e64 v83, v83, s44
	global_store_dwordx4 v[94:95], v[80:83], off
	s_nop 4
	v_add_f32_e32 v89, v26, v90
	v_mul_f32_e64 v90, |v89|, s35
	v_exp_f32_e32 v118, v90
	v_min_f32_e32 v80, 0, v89
	v_add_f32_e32 v81, v27, v91
	v_mul_f32_e64 v82, |v81|, s35
	v_exp_f32_e32 v119, v82
	v_min_f32_e32 v81, 0, v81
	s_nop 0
	s_nop 0
	v_add_f32_e32 v89, v28, v92
	s_nop 0
	s_nop 0
	s_nop 0
	s_nop 0
	s_nop 0
	s_nop 0
	s_nop 0
	s_nop 0
	s_nop 0
	s_nop 0
	s_nop 0
	s_nop 0
	s_nop 0
	s_nop 0
	s_nop 0
	s_nop 0
	s_nop 0
	v_mul_f32_e64 v90, |v89|, s35
	s_nop 1
	s_nop 1
	s_nop 1
	s_nop 1
	s_nop 1
	s_nop 1
	s_nop 1
	v_add_f32_e32 v83, 1.0, v119
	v_log_f32_e32 v83, v83
	s_nop 1
	v_mul_f32_e32 v83, 0x3f317218, v83
	s_nop 1
	v_exp_f32_e32 v119, v90
	s_nop 1
	s_nop 1
	v_add_f32_e32 v82, 1.0, v118
	v_log_f32_e32 v82, v82
	s_nop 1
	v_mul_f32_e32 v82, 0x3f317218, v82
	s_nop 1
	v_pk_add_f32 v[80:81], v[80:81], v[82:83] neg_lo:[0,1] neg_hi:[0,1]
	v_min_f32_e32 v82, 0, v89
	v_add_f32_e32 v83, v29, v93
	v_mul_f32_e64 v90, |v83|, s35
	v_exp_f32_e32 v118, v90
	v_min_f32_e32 v83, 0, v83
	v_pk_mul_f32 v[80:81], v[80:81], s[44:45] op_sel_hi:[1,0]
	s_nop 0
	s_nop 0
	s_nop 0
	s_nop 0
	s_nop 0
	s_nop 0
	s_nop 0
	s_nop 0
	s_nop 0
	s_nop 0
	s_nop 0
	s_nop 0
	s_nop 0
	s_nop 0
	s_nop 0
	s_nop 0
	s_nop 0
	s_nop 0
	v_lshl_add_u64 v[94:95], s[12:13], 2, v[70:71]
	s_nop 0
	s_nop 1
	s_nop 1
	s_nop 1
	s_nop 1
	s_nop 1
	s_nop 1
	s_nop 1
	v_add_f32_e32 v91, 1.0, v118
	v_log_f32_e32 v91, v91
	s_nop 1
	v_mul_f32_e32 v91, 0x3f317218, v91
	s_nop 1
	s_nop 1
	s_nop 1
	v_add_f32_e32 v90, 1.0, v119
	v_log_f32_e32 v90, v90
	s_nop 1
	v_mul_f32_e32 v90, 0x3f317218, v90
	s_nop 1
	v_pk_add_f32 v[82:83], v[82:83], v[90:91] neg_lo:[0,1] neg_hi:[0,1]
	v_mfma_f32_16x16x32_bf16 v[90:93], v[18:21], v[66:69], 0
	v_mul_f32_e64 v82, v82, s44
	v_mul_f32_e64 v83, v83, s44
	global_store_dwordx4 v[94:95], v[80:83], off
	s_nop 4
	v_add_f32_e32 v89, v30, v90
	v_mul_f32_e64 v90, |v89|, s35
	v_exp_f32_e32 v118, v90
	v_min_f32_e32 v80, 0, v89
	v_add_f32_e32 v81, v31, v91
	v_mul_f32_e64 v82, |v81|, s35
	v_exp_f32_e32 v119, v82
	v_min_f32_e32 v81, 0, v81
	s_nop 0
	s_nop 0
	v_add_f32_e32 v89, v32, v92
	s_nop 0
	s_nop 0
	s_nop 0
	s_nop 0
	s_nop 0
	s_nop 0
	s_nop 0
	s_nop 0
	s_nop 0
	s_nop 0
	s_nop 0
	s_nop 0
	s_nop 0
	s_nop 0
	s_nop 0
	s_nop 0
	s_nop 0
	v_mul_f32_e64 v90, |v89|, s35
	s_nop 1
	s_nop 1
	s_nop 1
	s_nop 1
	s_nop 1
	s_nop 1
	s_nop 1
	v_add_f32_e32 v83, 1.0, v119
	v_log_f32_e32 v83, v83
	s_nop 1
	v_mul_f32_e32 v83, 0x3f317218, v83
	s_nop 1
	v_exp_f32_e32 v119, v90
	s_nop 1
	s_nop 1
	v_add_f32_e32 v82, 1.0, v118
	v_log_f32_e32 v82, v82
	s_nop 1
	v_mul_f32_e32 v82, 0x3f317218, v82
	s_nop 1
	v_pk_add_f32 v[80:81], v[80:81], v[82:83] neg_lo:[0,1] neg_hi:[0,1]
	v_min_f32_e32 v82, 0, v89
	v_add_f32_e32 v83, v33, v93
	v_mul_f32_e64 v90, |v83|, s35
	v_exp_f32_e32 v118, v90
	v_min_f32_e32 v83, 0, v83
	v_pk_mul_f32 v[80:81], v[80:81], s[44:45] op_sel_hi:[1,0]
	s_nop 0
	s_nop 0
	s_nop 0
	s_nop 0
	s_nop 0
	s_nop 0
	s_nop 0
	s_nop 0
	s_nop 0
	s_nop 0
	s_nop 0
	s_nop 0
	s_nop 0
	s_nop 0
	s_nop 0
	s_nop 0
	s_nop 0
	s_nop 0
	v_lshl_add_u64 v[94:95], s[14:15], 2, v[70:71]
	s_nop 0
	s_nop 1
	s_nop 1
	s_nop 1
	s_nop 1
	s_nop 1
	s_nop 1
	s_nop 1
	v_add_f32_e32 v91, 1.0, v118
	v_log_f32_e32 v91, v91
	s_nop 1
	v_mul_f32_e32 v91, 0x3f317218, v91
	s_nop 1
	s_nop 1
	s_nop 1
	v_add_f32_e32 v90, 1.0, v119
	v_log_f32_e32 v90, v90
	s_nop 1
	v_mul_f32_e32 v90, 0x3f317218, v90
	s_nop 1
	v_pk_add_f32 v[82:83], v[82:83], v[90:91] neg_lo:[0,1] neg_hi:[0,1]
	v_mfma_f32_16x16x32_bf16 v[90:93], v[38:41], v[66:69], 0
	v_mul_f32_e64 v82, v82, s44
	v_mul_f32_e64 v83, v83, s44
	global_store_dwordx4 v[94:95], v[80:83], off
	s_nop 4
	v_add_f32_e32 v89, v42, v90
	v_mul_f32_e64 v90, |v89|, s35
	v_exp_f32_e32 v118, v90
	v_min_f32_e32 v80, 0, v89
	v_add_f32_e32 v81, v43, v91
	v_mul_f32_e64 v82, |v81|, s35
	v_exp_f32_e32 v119, v82
	v_min_f32_e32 v81, 0, v81
	s_nop 0
	s_nop 0
	v_add_f32_e32 v89, v44, v92
	s_nop 0
	s_nop 0
	s_nop 0
	s_nop 0
	s_nop 0
	s_nop 0
	s_nop 0
	s_nop 0
	s_nop 0
	s_nop 0
	s_nop 0
	s_nop 0
	s_nop 0
	s_nop 0
	s_nop 0
	s_nop 0
	s_nop 0
	v_mul_f32_e64 v90, |v89|, s35
	s_nop 1
	s_nop 1
	s_nop 1
	s_nop 1
	s_nop 1
	s_nop 1
	s_nop 1
	v_add_f32_e32 v83, 1.0, v119
	v_log_f32_e32 v83, v83
	s_nop 1
	v_mul_f32_e32 v83, 0x3f317218, v83
	s_nop 1
	v_exp_f32_e32 v119, v90
	s_nop 1
	s_nop 1
	v_add_f32_e32 v82, 1.0, v118
	v_log_f32_e32 v82, v82
	s_nop 1
	v_mul_f32_e32 v82, 0x3f317218, v82
	s_nop 1
	v_pk_add_f32 v[80:81], v[80:81], v[82:83] neg_lo:[0,1] neg_hi:[0,1]
	v_min_f32_e32 v82, 0, v89
	v_add_f32_e32 v83, v45, v93
	v_mul_f32_e64 v90, |v83|, s35
	v_exp_f32_e32 v118, v90
	v_min_f32_e32 v83, 0, v83
	v_pk_mul_f32 v[80:81], v[80:81], s[44:45] op_sel_hi:[1,0]
	s_nop 0
	s_nop 0
	s_nop 0
	s_nop 0
	s_nop 0
	s_nop 0
	s_nop 0
	s_nop 0
	s_nop 0
	s_nop 0
	s_nop 0
	s_nop 0
	s_nop 0
	s_nop 0
	s_nop 0
	s_nop 0
	s_nop 0
	s_nop 0
	v_lshl_add_u64 v[94:95], s[16:17], 2, v[70:71]
	s_nop 0
	s_nop 1
	s_nop 1
	s_nop 1
	s_nop 1
	s_nop 1
	s_nop 1
	s_nop 1
	v_add_f32_e32 v91, 1.0, v118
	v_log_f32_e32 v91, v91
	s_nop 1
	v_mul_f32_e32 v91, 0x3f317218, v91
	s_nop 1
	s_nop 1
	s_nop 1
	v_add_f32_e32 v90, 1.0, v119
	v_log_f32_e32 v90, v90
	s_nop 1
	v_mul_f32_e32 v90, 0x3f317218, v90
	s_nop 1
	v_pk_add_f32 v[82:83], v[82:83], v[90:91] neg_lo:[0,1] neg_hi:[0,1]
	v_mfma_f32_16x16x32_bf16 v[90:93], v[34:37], v[66:69], 0
	v_mul_f32_e64 v82, v82, s44
	v_mul_f32_e64 v83, v83, s44
	global_store_dwordx4 v[94:95], v[80:83], off
	s_nop 4
	v_add_f32_e32 v89, v46, v90
	v_mul_f32_e64 v90, |v89|, s35
	v_exp_f32_e32 v118, v90
	v_min_f32_e32 v80, 0, v89
	v_add_f32_e32 v81, v47, v91
	v_mul_f32_e64 v82, |v81|, s35
	v_exp_f32_e32 v119, v82
	v_min_f32_e32 v81, 0, v81
	s_nop 0
	s_nop 0
	v_add_f32_e32 v89, v48, v92
	s_nop 0
	s_nop 0
	s_nop 0
	s_nop 0
	s_nop 0
	s_nop 0
	s_nop 0
	s_nop 0
	s_nop 0
	s_nop 0
	s_nop 0
	s_nop 0
	s_nop 0
	s_nop 0
	s_nop 0
	s_nop 0
	s_nop 0
	v_mul_f32_e64 v90, |v89|, s35
	s_nop 1
	s_nop 1
	s_nop 1
	s_nop 1
	s_nop 1
	s_nop 1
	s_nop 1
	v_add_f32_e32 v83, 1.0, v119
	v_log_f32_e32 v83, v83
	s_nop 1
	v_mul_f32_e32 v83, 0x3f317218, v83
	s_nop 1
	v_exp_f32_e32 v119, v90
	s_nop 1
	s_nop 1
	v_add_f32_e32 v82, 1.0, v118
	v_log_f32_e32 v82, v82
	s_nop 1
	v_mul_f32_e32 v82, 0x3f317218, v82
	s_nop 1
	v_pk_add_f32 v[80:81], v[80:81], v[82:83] neg_lo:[0,1] neg_hi:[0,1]
	v_min_f32_e32 v82, 0, v89
	v_add_f32_e32 v83, v49, v93
	v_mul_f32_e64 v90, |v83|, s35
	v_exp_f32_e32 v118, v90
	v_min_f32_e32 v83, 0, v83
	v_pk_mul_f32 v[80:81], v[80:81], s[44:45] op_sel_hi:[1,0]
	s_nop 0
	s_nop 0
	s_nop 0
	s_nop 0
	s_nop 0
	s_nop 0
	s_nop 0
	s_nop 0
	s_nop 0
	s_nop 0
	s_nop 0
	s_nop 0
	s_nop 0
	s_nop 0
	s_nop 0
	s_nop 0
	s_nop 0
	s_nop 0
	v_lshl_add_u64 v[94:95], s[18:19], 2, v[70:71]
	s_nop 0
	s_nop 1
	s_nop 1
	s_nop 1
	s_nop 1
	s_nop 1
	s_nop 1
	s_nop 1
	v_add_f32_e32 v91, 1.0, v118
	v_log_f32_e32 v91, v91
	s_nop 1
	v_mul_f32_e32 v91, 0x3f317218, v91
	s_nop 1
	s_nop 1
	s_nop 1
	v_add_f32_e32 v90, 1.0, v119
	v_log_f32_e32 v90, v90
	s_nop 1
	v_mul_f32_e32 v90, 0x3f317218, v90
	s_nop 1
	v_pk_add_f32 v[82:83], v[82:83], v[90:91] neg_lo:[0,1] neg_hi:[0,1]
	v_mfma_f32_16x16x32_bf16 v[90:93], v[54:57], v[66:69], 0
	v_mul_f32_e64 v82, v82, s44
	v_mul_f32_e64 v83, v83, s44
	global_store_dwordx4 v[94:95], v[80:83], off
	v_mfma_f32_16x16x32_bf16 v[66:69], v[50:53], v[66:69], 0
	s_nop 3
	v_add_f32_e32 v89, v58, v90
	v_mul_f32_e64 v90, |v89|, s35
	v_exp_f32_e32 v118, v90
	v_min_f32_e32 v80, 0, v89
	v_add_f32_e32 v66, v62, v66
	v_add_f32_e32 v67, v63, v67
	v_add_f32_e32 v81, v59, v91
	v_mul_f32_e64 v82, |v81|, s35
	v_exp_f32_e32 v119, v82
	v_min_f32_e32 v81, 0, v81
	v_add_f32_e32 v68, v64, v68
	v_add_f32_e32 v69, v65, v69
	v_add_f32_e32 v89, v60, v92
	s_nop 0
	s_nop 0
	s_nop 0
	s_nop 0
	s_nop 0
	s_nop 0
	s_nop 0
	s_nop 0
	s_nop 0
	s_nop 0
	s_nop 0
	s_nop 0
	s_nop 0
	s_nop 0
	s_nop 0
	s_nop 0
	s_nop 0
	v_mul_f32_e64 v90, |v89|, s35
	s_nop 1
	s_nop 1
	s_nop 1
	s_nop 1
	s_nop 1
	s_nop 1
	s_nop 1
	v_add_f32_e32 v83, 1.0, v119
	v_log_f32_e32 v83, v83
	s_nop 1
	v_mul_f32_e32 v83, 0x3f317218, v83
	s_nop 1
	v_exp_f32_e32 v119, v90
	s_nop 1
	s_nop 1
	v_add_f32_e32 v82, 1.0, v118
	v_log_f32_e32 v82, v82
	s_nop 1
	v_mul_f32_e32 v82, 0x3f317218, v82
	s_nop 1
	v_pk_add_f32 v[80:81], v[80:81], v[82:83] neg_lo:[0,1] neg_hi:[0,1]
	v_min_f32_e32 v82, 0, v89
	v_add_f32_e32 v83, v61, v93
	v_mul_f32_e64 v90, |v83|, s35
	v_exp_f32_e32 v118, v90
	v_min_f32_e32 v83, 0, v83
	v_pk_mul_f32 v[80:81], v[80:81], s[44:45] op_sel_hi:[1,0]
	s_nop 0
	s_nop 0
	s_nop 0
	s_nop 0
	s_nop 0
	s_nop 0
	s_nop 0
	s_nop 0
	s_nop 0
	s_nop 0
	s_nop 0
	s_nop 0
	s_nop 0
	s_nop 0
	s_nop 0
	s_nop 0
	s_nop 0
	s_nop 0
	s_nop 0
	s_nop 0
	s_nop 1
	s_nop 1
	s_nop 1
	s_nop 1
	s_nop 1
	s_nop 1
	s_nop 1
	v_add_f32_e32 v91, 1.0, v118
	v_log_f32_e32 v91, v91
	s_nop 1
	v_mul_f32_e32 v91, 0x3f317218, v91
	s_nop 1
	s_nop 1
	s_nop 1
	v_add_f32_e32 v90, 1.0, v119
	v_log_f32_e32 v90, v90
	s_nop 1
	v_mul_f32_e32 v90, 0x3f317218, v90
	s_nop 1
	v_mul_f32_e64 v89, |v66|, s35
	v_exp_f32_e32 v89, v89
	v_pk_add_f32 v[82:83], v[82:83], v[90:91] neg_lo:[0,1] neg_hi:[0,1]
	v_lshl_add_u64 v[90:91], s[20:21], 2, v[70:71]
	v_pk_mul_f32 v[82:83], v[82:83], s[44:45] op_sel_hi:[1,0]
	global_store_dwordx4 v[90:91], v[80:83], off
	v_min_f32_e32 v66, 0, v66
	v_lshl_add_u64 v[70:71], s[22:23], 2, v[70:71]
	v_mul_f32_e64 v80, |v67|, s35
	v_exp_f32_e32 v114, v80
	v_min_f32_e32 v67, 0, v67
	s_nop 0
	s_nop 1
	s_nop 0
	s_nop 0
	s_nop 0
	s_nop 0
	s_nop 0
	s_nop 0
	s_nop 0
	s_nop 0
	s_nop 0
	s_nop 0
	s_nop 0
	s_nop 0
	s_nop 0
	s_nop 0
	s_nop 0
	s_nop 0
	s_nop 0
	v_mul_f32_e64 v82, |v68|, s35
	v_min_f32_e32 v68, 0, v68
	s_nop 0
	s_nop 1
	s_nop 1
	s_nop 1
	s_nop 1
	s_nop 1
	s_nop 1
	v_add_f32_e32 v81, 1.0, v114
	v_log_f32_e32 v81, v81
	s_nop 1
	v_mul_f32_e32 v81, 0x3f317218, v81
	s_nop 1
	v_exp_f32_e32 v114, v82
	s_nop 0
	s_nop 1
	v_add_f32_e32 v80, 1.0, v89
	v_log_f32_e32 v80, v80
	s_nop 1
	v_mul_f32_e32 v80, 0x3f317218, v80
	s_nop 1
	v_pk_add_f32 v[66:67], v[66:67], v[80:81] neg_lo:[0,1] neg_hi:[0,1]
	v_mul_f32_e64 v80, |v69|, s35
	v_exp_f32_e32 v115, v80
	v_min_f32_e32 v69, 0, v69
	v_pk_mul_f32 v[66:67], v[66:67], s[44:45] op_sel_hi:[1,0]
	s_nop 0
	s_nop 0
	s_nop 0
	s_nop 0
	s_nop 0
	s_nop 0
	s_nop 0
	s_nop 0
	s_nop 0
	s_nop 0
	s_nop 0
	s_nop 0
	s_nop 0
	s_nop 0
	s_nop 0
	s_nop 0
	s_nop 0
	s_nop 0
	s_nop 0
	s_nop 0
	s_nop 1
	s_nop 1
	s_nop 1
	s_nop 1
	s_nop 1
	s_nop 1
	s_nop 1
	v_add_f32_e32 v79, 1.0, v115
	v_log_f32_e32 v79, v79
	s_nop 1
	v_mul_f32_e32 v79, 0x3f317218, v79
	s_nop 1
	v_cmp_lt_f32_e64 vcc, |v114|, s45
	s_nop 1
	s_nop 1
	v_add_f32_e32 v78, 1.0, v114
	v_log_f32_e32 v78, v78
	s_nop 1
	v_mul_f32_e32 v78, 0x3f317218, v78
	s_nop 1
	v_pk_add_f32 v[68:69], v[68:69], v[78:79] neg_lo:[0,1] neg_hi:[0,1]
	s_nop 0
	v_pk_mul_f32 v[68:69], v[68:69], s[44:45] op_sel_hi:[1,0]
	global_store_dwordx4 v[70:71], v[66:69], off
	s_barrier
	s_cbranch_scc0 .LBB0_161

.LBB0_153:
	s_nop 0
	v_mov_b32_e32 v66, 0
	v_mov_b32_e32 v68, 0
	v_mov_b32_e32 v69, 0
	v_mov_b32_e32 v70, 0
	v_mov_b32_e32 v71, 0
	s_waitcnt lgkmcnt(0)
	s_barrier
	s_and_saveexec_b64 s[72:73], s[4:5]
	ds_read_b128 v[68:71], v72
	s_or_b64 exec, exec, s[72:73]
	s_waitcnt lgkmcnt(0)
	v_mfma_f32_16x16x32_bf16 v[80:83], v[6:9], v[68:71], 0
	s_ashr_i32 s71, s70, 31
	s_lshl_b64 s[72:73], s[70:71], 18
	v_lshl_or_b32 v78, v130, 12, s72
	s_nop 4
	v_add_f32_e32 v67, v10, v80
	v_mul_f32_e64 v79, |v67|, s35
	v_exp_f32_e32 v89, v79
	v_min_f32_e32 v90, 0, v67
	v_add_f32_e32 v82, v12, v82
	v_add_f32_e32 v83, v13, v83
	v_add_f32_e32 v91, v11, v81
	v_mul_f32_e64 v80, |v91|, s35
	v_exp_f32_e32 v118, v80
	v_min_f32_e32 v91, 0, v91
	v_mov_b32_e32 v79, s73
	v_lshl_add_u64 v[78:79], v[74:75], 0, v[78:79]
	s_nop 0
	s_nop 0
	s_nop 0
	s_nop 0
	s_nop 0
	s_nop 0
	s_nop 0
	s_nop 0
	s_nop 0
	s_nop 0
	s_nop 0
	s_nop 0
	s_nop 0
	s_nop 0
	s_nop 0
	s_nop 0
	s_nop 0
	s_nop 0
	s_nop 0
	s_nop 1
	s_nop 1
	s_nop 1
	s_nop 1
	s_nop 1
	s_nop 1
	s_nop 1
	v_add_f32_e32 v93, 1.0, v118
	v_log_f32_e32 v93, v93
	s_nop 1
	v_mul_f32_e32 v93, 0x3f317218, v93
	s_nop 1
	v_mul_f32_e64 v92, |v82|, s35
	v_exp_f32_e32 v120, v92
	v_min_f32_e32 v82, 0, v82
	s_nop 0
	s_nop 1
	v_add_f32_e32 v92, 1.0, v89
	v_log_f32_e32 v92, v92
	s_nop 1
	v_mul_f32_e32 v92, 0x3f317218, v92
	s_nop 1
	v_pk_add_f32 v[90:91], v[90:91], v[92:93] neg_lo:[0,1] neg_hi:[0,1]
	v_mul_f32_e64 v92, |v83|, s35
	v_exp_f32_e32 v121, v92
	v_min_f32_e32 v83, 0, v83
	v_pk_mul_f32 v[90:91], v[90:91], s[44:45] op_sel_hi:[1,0]
	s_nop 0
	s_nop 0
	s_nop 0
	s_nop 0
	s_nop 0
	s_nop 0
	s_nop 0
	s_nop 0
	s_nop 0
	s_nop 0
	s_nop 0
	s_nop 0
	s_nop 0
	s_nop 0
	s_nop 0
	s_nop 0
	s_nop 0
	s_nop 0
	s_nop 0
	v_mfma_f32_16x16x32_bf16 v[94:97], v[2:5], v[68:71], 0
	s_nop 1
	s_nop 1
	s_nop 1
	s_nop 1
	s_nop 1
	s_nop 1
	s_nop 1
	v_add_f32_e32 v93, 1.0, v121
	v_log_f32_e32 v93, v93
	s_nop 1
	v_mul_f32_e32 v93, 0x3f317218, v93
	s_nop 1
	s_nop 1
	s_nop 1
	v_add_f32_e32 v92, 1.0, v120
	v_log_f32_e32 v92, v92
	s_nop 1
	v_mul_f32_e32 v92, 0x3f317218, v92
	s_nop 1
	v_pk_add_f32 v[82:83], v[82:83], v[92:93] neg_lo:[0,1] neg_hi:[0,1]
	v_add_f32_e32 v67, v14, v94
	v_pk_mul_f32 v[92:93], v[82:83], s[44:45] op_sel_hi:[1,0]
	v_mul_f32_e64 v82, |v67|, s35
	v_exp_f32_e32 v89, v82
	v_lshl_add_u64 v[82:83], s[2:3], 2, v[78:79]
	global_store_dwordx4 v[82:83], v[90:93], off
	s_nop 1
	v_min_f32_e32 v90, 0, v67
	v_add_f32_e32 v91, v15, v95
	v_mul_f32_e64 v92, |v91|, s35
	v_exp_f32_e32 v122, v92
	v_min_f32_e32 v91, 0, v91
	s_nop 0
	s_nop 0
	s_nop 0
	s_nop 0
	s_nop 0
	s_nop 0
	s_nop 0
	s_nop 0
	s_nop 0
	s_nop 0
	s_nop 0
	s_nop 0
	s_nop 0
	s_nop 0
	s_nop 0
	s_nop 0
	s_nop 0
	s_nop 0
	s_nop 0
	s_nop 0
	v_add_f32_e32 v94, v16, v96
	s_nop 1
	s_nop 1
	s_nop 1
	s_nop 1
	s_nop 1
	s_nop 1
	s_nop 1
	v_add_f32_e32 v93, 1.0, v122
	v_log_f32_e32 v93, v93
	s_nop 1
	v_mul_f32_e32 v93, 0x3f317218, v93
	s_nop 1
	v_mul_f32_e64 v92, |v94|, s35
	v_exp_f32_e32 v122, v92
	s_nop 1
	s_nop 1
	v_add_f32_e32 v92, 1.0, v89
	v_log_f32_e32 v92, v92
	s_nop 1
	v_mul_f32_e32 v92, 0x3f317218, v92
	s_nop 1
	v_pk_add_f32 v[90:91], v[90:91], v[92:93] neg_lo:[0,1] neg_hi:[0,1]
	v_add_f32_e32 v93, v17, v97
	v_min_f32_e32 v92, 0, v94
	v_mul_f32_e64 v94, |v93|, s35
	v_exp_f32_e32 v123, v94
	v_min_f32_e32 v93, 0, v93
	v_pk_mul_f32 v[90:91], v[90:91], s[44:45] op_sel_hi:[1,0]
	s_nop 0
	s_nop 0
	s_nop 0
	s_nop 0
	s_nop 0
	s_nop 0
	s_nop 0
	s_nop 0
	s_nop 0
	s_nop 0
	s_nop 0
	s_nop 0
	s_nop 0
	s_nop 0
	s_nop 0
	s_nop 0
	s_nop 0
	s_nop 0
	s_nop 0
	s_nop 0
	s_nop 1
	s_nop 1
	s_nop 1
	s_nop 1
	s_nop 1
	s_nop 1
	s_nop 1
	v_add_f32_e32 v95, 1.0, v123
	v_log_f32_e32 v95, v95
	s_nop 1
	v_mul_f32_e32 v95, 0x3f317218, v95
	s_nop 1
	s_nop 1
	s_nop 1
	v_add_f32_e32 v94, 1.0, v122
	v_log_f32_e32 v94, v94
	s_nop 1
	v_mul_f32_e32 v94, 0x3f317218, v94
	s_nop 1
	v_pk_add_f32 v[92:93], v[92:93], v[94:95] neg_lo:[0,1] neg_hi:[0,1]
	v_mfma_f32_16x16x32_bf16 v[94:97], v[22:25], v[68:71], 0
	v_mul_f32_e64 v92, v92, s44
	v_mul_f32_e64 v93, v93, s44
	global_store_dwordx4 v[82:83], v[90:93], off offset:64
	s_nop 4
	v_add_f32_e32 v67, v26, v94
	v_mul_f32_e64 v89, |v67|, s35
	v_exp_f32_e32 v89, v89
	v_min_f32_e32 v90, 0, v67
	v_add_f32_e32 v91, v27, v95
	v_mul_f32_e64 v92, |v91|, s35
	v_exp_f32_e32 v122, v92
	v_min_f32_e32 v91, 0, v91
	s_nop 0
	s_nop 0
	s_nop 0
	s_nop 0
	s_nop 0
	s_nop 0
	s_nop 0
	s_nop 0
	s_nop 0
	s_nop 0
	s_nop 0
	s_nop 0
	s_nop 0
	s_nop 0
	s_nop 0
	s_nop 0
	s_nop 0
	s_nop 0
	s_nop 0
	s_nop 0
	v_add_f32_e32 v94, v28, v96
	s_nop 1
	s_nop 1
	s_nop 1
	s_nop 1
	s_nop 1
	s_nop 1
	s_nop 1
	v_add_f32_e32 v93, 1.0, v122
	v_log_f32_e32 v93, v93
	s_nop 1
	v_mul_f32_e32 v93, 0x3f317218, v93
	s_nop 1
	v_mul_f32_e64 v92, |v94|, s35
	v_exp_f32_e32 v122, v92
	s_nop 1
	s_nop 1
	v_add_f32_e32 v92, 1.0, v89
	v_log_f32_e32 v92, v92
	s_nop 1
	v_mul_f32_e32 v92, 0x3f317218, v92
	s_nop 1
	v_pk_add_f32 v[90:91], v[90:91], v[92:93] neg_lo:[0,1] neg_hi:[0,1]
	v_add_f32_e32 v93, v29, v97
	v_min_f32_e32 v92, 0, v94
	v_mul_f32_e64 v94, |v93|, s35
	v_exp_f32_e32 v123, v94
	v_min_f32_e32 v93, 0, v93
	v_pk_mul_f32 v[90:91], v[90:91], s[44:45] op_sel_hi:[1,0]
	s_nop 0
	s_nop 0
	s_nop 0
	s_nop 0
	s_nop 0
	s_nop 0
	s_nop 0
	s_nop 0
	s_nop 0
	s_nop 0
	s_nop 0
	s_nop 0
	s_nop 0
	s_nop 0
	s_nop 0
	s_nop 0
	s_nop 0
	s_nop 0
	s_nop 0
	s_nop 0
	s_nop 1
	s_nop 1
	s_nop 1
	s_nop 1
	s_nop 1
	s_nop 1
	s_nop 1
	v_add_f32_e32 v95, 1.0, v123
	v_log_f32_e32 v95, v95
	s_nop 1
	v_mul_f32_e32 v95, 0x3f317218, v95
	s_nop 1
	s_nop 1
	s_nop 1
	v_add_f32_e32 v94, 1.0, v122
	v_log_f32_e32 v94, v94
	s_nop 1
	v_mul_f32_e32 v94, 0x3f317218, v94
	s_nop 1
	v_pk_add_f32 v[92:93], v[92:93], v[94:95] neg_lo:[0,1] neg_hi:[0,1]
	v_mfma_f32_16x16x32_bf16 v[94:97], v[18:21], v[68:71], 0
	v_mul_f32_e64 v92, v92, s44
	v_mul_f32_e64 v93, v93, s44
	global_store_dwordx4 v[82:83], v[90:93], off offset:128
	s_nop 4
	v_add_f32_e32 v67, v30, v94
	v_mul_f32_e64 v89, |v67|, s35
	v_exp_f32_e32 v89, v89
	v_min_f32_e32 v90, 0, v67
	v_add_f32_e32 v91, v31, v95
	v_mul_f32_e64 v92, |v91|, s35
	v_exp_f32_e32 v122, v92
	v_min_f32_e32 v91, 0, v91
	s_nop 0
	s_nop 0
	s_nop 0
	s_nop 0
	s_nop 0
	s_nop 0
	s_nop 0
	s_nop 0
	s_nop 0
	s_nop 0
	s_nop 0
	s_nop 0
	s_nop 0
	s_nop 0
	s_nop 0
	s_nop 0
	s_nop 0
	s_nop 0
	s_nop 0
	s_nop 0
	v_add_f32_e32 v94, v32, v96
	s_nop 1
	s_nop 1
	s_nop 1
	s_nop 1
	s_nop 1
	s_nop 1
	s_nop 1
	v_add_f32_e32 v93, 1.0, v122
	v_log_f32_e32 v93, v93
	s_nop 1
	v_mul_f32_e32 v93, 0x3f317218, v93
	s_nop 1
	v_mul_f32_e64 v92, |v94|, s35
	v_exp_f32_e32 v122, v92
	s_nop 1
	s_nop 1
	v_add_f32_e32 v92, 1.0, v89
	v_log_f32_e32 v92, v92
	s_nop 1
	v_mul_f32_e32 v92, 0x3f317218, v92
	s_nop 1
	v_pk_add_f32 v[90:91], v[90:91], v[92:93] neg_lo:[0,1] neg_hi:[0,1]
	v_add_f32_e32 v93, v33, v97
	v_min_f32_e32 v92, 0, v94
	v_mul_f32_e64 v94, |v93|, s35
	v_exp_f32_e32 v123, v94
	v_min_f32_e32 v93, 0, v93
	v_pk_mul_f32 v[90:91], v[90:91], s[44:45] op_sel_hi:[1,0]
	s_nop 0
	s_nop 0
	s_nop 0
	s_nop 0
	s_nop 0
	s_nop 0
	s_nop 0
	s_nop 0
	s_nop 0
	s_nop 0
	s_nop 0
	s_nop 0
	s_nop 0
	s_nop 0
	s_nop 0
	s_nop 0
	s_nop 0
	s_nop 0
	s_nop 0
	s_nop 0
	s_nop 1
	s_nop 1
	s_nop 1
	s_nop 1
	s_nop 1
	s_nop 1
	s_nop 1
	v_add_f32_e32 v95, 1.0, v123
	v_log_f32_e32 v95, v95
	s_nop 1
	v_mul_f32_e32 v95, 0x3f317218, v95
	s_nop 1
	s_nop 1
	s_nop 1
	v_add_f32_e32 v94, 1.0, v122
	v_log_f32_e32 v94, v94
	s_nop 1
	v_mul_f32_e32 v94, 0x3f317218, v94
	s_nop 1
	v_pk_add_f32 v[92:93], v[92:93], v[94:95] neg_lo:[0,1] neg_hi:[0,1]
	v_mfma_f32_16x16x32_bf16 v[94:97], v[38:41], v[68:71], 0
	v_mul_f32_e64 v92, v92, s44
	v_mul_f32_e64 v93, v93, s44
	global_store_dwordx4 v[82:83], v[90:93], off offset:192
	s_nop 4
	v_add_f32_e32 v67, v42, v94
	v_mul_f32_e64 v89, |v67|, s35
	v_exp_f32_e32 v89, v89
	v_min_f32_e32 v90, 0, v67
	v_add_f32_e32 v91, v43, v95
	v_mul_f32_e64 v92, |v91|, s35
	v_exp_f32_e32 v122, v92
	v_min_f32_e32 v91, 0, v91
	s_nop 0
	s_nop 0
	s_nop 0
	s_nop 0
	s_nop 0
	s_nop 0
	s_nop 0
	s_nop 0
	s_nop 0
	s_nop 0
	s_nop 0
	s_nop 0
	s_nop 0
	s_nop 0
	s_nop 0
	s_nop 0
	s_nop 0
	s_nop 0
	s_nop 0
	s_nop 0
	v_add_f32_e32 v94, v44, v96
	s_nop 1
	s_nop 1
	s_nop 1
	s_nop 1
	s_nop 1
	s_nop 1
	s_nop 1
	v_add_f32_e32 v93, 1.0, v122
	v_log_f32_e32 v93, v93
	s_nop 1
	v_mul_f32_e32 v93, 0x3f317218, v93
	s_nop 1
	v_mul_f32_e64 v92, |v94|, s35
	v_exp_f32_e32 v122, v92
	s_nop 1
	s_nop 1
	v_add_f32_e32 v92, 1.0, v89
	v_log_f32_e32 v92, v92
	s_nop 1
	v_mul_f32_e32 v92, 0x3f317218, v92
	s_nop 1
	v_pk_add_f32 v[90:91], v[90:91], v[92:93] neg_lo:[0,1] neg_hi:[0,1]
	v_add_f32_e32 v93, v45, v97
	v_min_f32_e32 v92, 0, v94
	v_mul_f32_e64 v94, |v93|, s35
	v_exp_f32_e32 v123, v94
	v_min_f32_e32 v93, 0, v93
	v_pk_mul_f32 v[90:91], v[90:91], s[44:45] op_sel_hi:[1,0]
	s_nop 0
	s_nop 0
	s_nop 0
	s_nop 0
	s_nop 0
	s_nop 0
	s_nop 0
	s_nop 0
	s_nop 0
	s_nop 0
	s_nop 0
	s_nop 0
	s_nop 0
	s_nop 0
	s_nop 0
	s_nop 0
	s_nop 0
	s_nop 0
	s_nop 0
	s_nop 0
	s_nop 1
	s_nop 1
	s_nop 1
	s_nop 1
	s_nop 1
	s_nop 1
	s_nop 1
	v_add_f32_e32 v95, 1.0, v123
	v_log_f32_e32 v95, v95
	s_nop 1
	v_mul_f32_e32 v95, 0x3f317218, v95
	s_nop 1
	s_nop 1
	s_nop 1
	v_add_f32_e32 v94, 1.0, v122
	v_log_f32_e32 v94, v94
	s_nop 1
	v_mul_f32_e32 v94, 0x3f317218, v94
	s_nop 1
	v_pk_add_f32 v[92:93], v[92:93], v[94:95] neg_lo:[0,1] neg_hi:[0,1]
	v_mfma_f32_16x16x32_bf16 v[94:97], v[34:37], v[68:71], 0
	v_mul_f32_e64 v92, v92, s44
	v_mul_f32_e64 v93, v93, s44
	global_store_dwordx4 v[82:83], v[90:93], off offset:256
	s_nop 4
	v_add_f32_e32 v67, v46, v94
	v_mul_f32_e64 v89, |v67|, s35
	v_exp_f32_e32 v89, v89
	v_min_f32_e32 v90, 0, v67
	v_add_f32_e32 v91, v47, v95
	v_mul_f32_e64 v92, |v91|, s35
	v_exp_f32_e32 v122, v92
	v_min_f32_e32 v91, 0, v91
	s_nop 0
	s_nop 0
	s_nop 0
	s_nop 0
	s_nop 0
	s_nop 0
	s_nop 0
	s_nop 0
	s_nop 0
	s_nop 0
	s_nop 0
	s_nop 0
	s_nop 0
	s_nop 0
	s_nop 0
	s_nop 0
	s_nop 0
	s_nop 0
	s_nop 0
	s_nop 0
	v_add_f32_e32 v94, v48, v96
	s_nop 1
	s_nop 1
	s_nop 1
	s_nop 1
	s_nop 1
	s_nop 1
	s_nop 1
	v_add_f32_e32 v93, 1.0, v122
	v_log_f32_e32 v93, v93
	s_nop 1
	v_mul_f32_e32 v93, 0x3f317218, v93
	s_nop 1
	v_mul_f32_e64 v92, |v94|, s35
	v_exp_f32_e32 v122, v92
	s_nop 1
	s_nop 1
	v_add_f32_e32 v92, 1.0, v89
	v_log_f32_e32 v92, v92
	s_nop 1
	v_mul_f32_e32 v92, 0x3f317218, v92
	s_nop 1
	v_pk_add_f32 v[90:91], v[90:91], v[92:93] neg_lo:[0,1] neg_hi:[0,1]
	v_add_f32_e32 v93, v49, v97
	v_min_f32_e32 v92, 0, v94
	v_mul_f32_e64 v94, |v93|, s35
	v_exp_f32_e32 v123, v94
	v_min_f32_e32 v93, 0, v93
	v_pk_mul_f32 v[90:91], v[90:91], s[44:45] op_sel_hi:[1,0]
	s_nop 0
	s_nop 0
	s_nop 0
	s_nop 0
	s_nop 0
	s_nop 0
	s_nop 0
	s_nop 0
	s_nop 0
	s_nop 0
	s_nop 0
	s_nop 0
	s_nop 0
	s_nop 0
	s_nop 0
	s_nop 0
	s_nop 0
	s_nop 0
	s_nop 0
	s_nop 0
	s_nop 1
	s_nop 1
	s_nop 1
	s_nop 1
	s_nop 1
	s_nop 1
	s_nop 1
	v_add_f32_e32 v95, 1.0, v123
	v_log_f32_e32 v95, v95
	s_nop 1
	v_mul_f32_e32 v95, 0x3f317218, v95
	s_nop 1
	s_nop 1
	s_nop 1
	v_add_f32_e32 v94, 1.0, v122
	v_log_f32_e32 v94, v94
	s_nop 1
	v_mul_f32_e32 v94, 0x3f317218, v94
	s_nop 1
	v_pk_add_f32 v[92:93], v[92:93], v[94:95] neg_lo:[0,1] neg_hi:[0,1]
	v_mfma_f32_16x16x32_bf16 v[94:97], v[54:57], v[68:71], 0
	v_mul_f32_e64 v92, v92, s44
	v_mul_f32_e64 v93, v93, s44
	global_store_dwordx4 v[82:83], v[90:93], off offset:320
	v_mfma_f32_16x16x32_bf16 v[68:71], v[50:53], v[68:71], 0
	s_nop 3
	v_add_f32_e32 v67, v58, v94
	v_mul_f32_e64 v89, |v67|, s35
	v_exp_f32_e32 v89, v89
	v_min_f32_e32 v90, 0, v67
	v_add_f32_e32 v69, v63, v69
	v_add_f32_e32 v70, v64, v70
	v_add_f32_e32 v91, v59, v95
	v_mul_f32_e64 v92, |v91|, s35
	v_exp_f32_e32 v122, v92
	v_min_f32_e32 v91, 0, v91
	v_add_f32_e32 v71, v65, v71
	s_nop 0
	s_nop 0
	s_nop 0
	s_nop 0
	s_nop 0
	s_nop 0
	s_nop 0
	s_nop 0
	s_nop 0
	s_nop 0
	s_nop 0
	s_nop 0
	s_nop 0
	s_nop 0
	s_nop 0
	s_nop 0
	s_nop 0
	s_nop 0
	s_nop 0
	v_add_f32_e32 v94, v60, v96
	s_nop 1
	s_nop 1
	s_nop 1
	s_nop 1
	s_nop 1
	s_nop 1
	s_nop 1
	v_add_f32_e32 v93, 1.0, v122
	v_log_f32_e32 v93, v93
	s_nop 1
	v_mul_f32_e32 v93, 0x3f317218, v93
	s_nop 1
	v_mul_f32_e64 v92, |v94|, s35
	v_exp_f32_e32 v122, v92
	s_nop 1
	s_nop 1
	v_add_f32_e32 v92, 1.0, v89
	v_log_f32_e32 v92, v92
	s_nop 1
	v_mul_f32_e32 v92, 0x3f317218, v92
	s_nop 1
	v_pk_add_f32 v[90:91], v[90:91], v[92:93] neg_lo:[0,1] neg_hi:[0,1]
	v_add_f32_e32 v93, v61, v97
	v_min_f32_e32 v92, 0, v94
	v_mul_f32_e64 v94, |v93|, s35
	v_exp_f32_e32 v123, v94
	v_min_f32_e32 v93, 0, v93
	v_pk_mul_f32 v[90:91], v[90:91], s[44:45] op_sel_hi:[1,0]
	s_nop 0
	s_nop 0
	s_nop 0
	s_nop 0
	s_nop 0
	s_nop 0
	s_nop 0
	s_nop 0
	s_nop 0
	s_nop 0
	s_nop 0
	s_nop 0
	s_nop 0
	s_nop 0
	s_nop 0
	s_nop 0
	s_nop 0
	s_nop 0
	s_nop 0
	s_nop 0
	s_nop 1
	s_nop 1
	s_nop 1
	s_nop 1
	s_nop 1
	s_nop 1
	s_nop 1
	v_add_f32_e32 v95, 1.0, v123
	v_log_f32_e32 v95, v95
	s_nop 1
	v_mul_f32_e32 v95, 0x3f317218, v95
	s_nop 1
	s_nop 1
	s_nop 1
	v_add_f32_e32 v94, 1.0, v122
	v_log_f32_e32 v94, v94
	s_nop 1
	v_mul_f32_e32 v94, 0x3f317218, v94
	s_nop 1
	v_add_f32_e32 v67, v62, v68
	v_mul_f32_e64 v68, |v67|, s35
	v_exp_f32_e32 v89, v68
	v_pk_add_f32 v[92:93], v[92:93], v[94:95] neg_lo:[0,1] neg_hi:[0,1]
	v_min_f32_e32 v68, 0, v67
	v_pk_mul_f32 v[92:93], v[92:93], s[44:45] op_sel_hi:[1,0]
	global_store_dwordx4 v[82:83], v[90:93], off offset:384
	s_nop 1
	v_mul_f32_e64 v90, |v69|, s35
	v_exp_f32_e32 v118, v90
	v_min_f32_e32 v69, 0, v69
	s_nop 0
	s_nop 0
	s_nop 0
	s_nop 0
	s_nop 0
	s_nop 0
	s_nop 0
	s_nop 0
	s_nop 0
	s_nop 0
	s_nop 0
	s_nop 0
	s_nop 0
	s_nop 0
	s_nop 0
	s_nop 0
	s_nop 0
	s_nop 0
	s_nop 0
	s_nop 0
	s_nop 0
	s_nop 1
	s_nop 1
	s_nop 1
	s_nop 1
	s_nop 1
	s_nop 1
	s_nop 1
	v_add_f32_e32 v91, 1.0, v118
	v_log_f32_e32 v91, v91
	s_nop 1
	v_mul_f32_e32 v91, 0x3f317218, v91
	s_nop 1
	v_mul_f32_e64 v90, |v70|, s35
	v_exp_f32_e32 v118, v90
	v_min_f32_e32 v70, 0, v70
	s_nop 0
	s_nop 1
	v_add_f32_e32 v90, 1.0, v89
	v_log_f32_e32 v90, v90
	s_nop 1
	v_mul_f32_e32 v90, 0x3f317218, v90
	s_nop 1
	v_pk_add_f32 v[68:69], v[68:69], v[90:91] neg_lo:[0,1] neg_hi:[0,1]
	v_mul_f32_e64 v90, |v71|, s35
	v_exp_f32_e32 v119, v90
	v_min_f32_e32 v71, 0, v71
	v_pk_mul_f32 v[68:69], v[68:69], s[44:45] op_sel_hi:[1,0]
	s_nop 0
	s_nop 0
	s_nop 0
	s_nop 0
	s_nop 0
	s_nop 0
	s_nop 0
	s_nop 0
	s_nop 0
	s_nop 0
	s_nop 0
	s_nop 0
	s_nop 0
	s_nop 0
	s_nop 0
	s_nop 0
	s_nop 0
	s_nop 0
	s_nop 0
	s_nop 0
	s_nop 0
	s_nop 1
	s_nop 1
	s_nop 1
	s_nop 1
	s_nop 1
	s_nop 1
	s_nop 1
	v_add_f32_e32 v81, 1.0, v119
	v_log_f32_e32 v81, v81
	s_nop 1
	v_mul_f32_e32 v81, 0x3f317218, v81
	s_nop 1
	s_nop 1
	s_nop 1
	v_add_f32_e32 v80, 1.0, v118
	v_log_f32_e32 v80, v80
	s_nop 1
	v_mul_f32_e32 v80, 0x3f317218, v80
	s_nop 1
	v_pk_add_f32 v[70:71], v[70:71], v[80:81] neg_lo:[0,1] neg_hi:[0,1]
	v_mov_b32_e32 v67, 0
	v_pk_mul_f32 v[70:71], v[70:71], s[44:45] op_sel_hi:[1,0]
	global_store_dwordx4 v[82:83], v[68:71], off offset:448
	s_nop 1
	v_mov_b32_e32 v68, 0
	v_mov_b32_e32 v69, 0
	s_and_saveexec_b64 s[72:73], s[4:5]
	ds_read_b128 v[66:69], v72 offset:512
	s_or_b64 exec, exec, s[72:73]
	s_waitcnt lgkmcnt(0)
	v_mfma_f32_16x16x32_bf16 v[80:83], v[6:9], v[66:69], 0
	v_lshl_add_u64 v[70:71], v[78:79], 0, s[62:63]
	s_nop 6
	v_add_f32_e32 v80, v10, v80
	v_mul_f32_e64 v89, |v80|, s35
	v_exp_f32_e32 v89, v89
	v_add_f32_e32 v91, v11, v81
	v_min_f32_e32 v90, 0, v80
	v_mul_f32_e64 v80, |v91|, s35
	v_exp_f32_e32 v118, v80
	v_add_f32_e32 v82, v12, v82
	v_min_f32_e32 v91, 0, v91
	v_add_f32_e32 v83, v13, v83
	s_nop 0
	s_nop 0
	s_nop 0
	s_nop 0
	s_nop 0
	s_nop 0
	s_nop 0
	s_nop 0
	s_nop 0
	s_nop 0
	s_nop 0
	s_nop 0
	s_nop 0
	s_nop 0
	s_nop 0
	s_nop 0
	s_nop 0
	v_mul_f32_e64 v94, |v82|, s35
	v_exp_f32_e32 v120, v94
	v_min_f32_e32 v82, 0, v82
	s_nop 0
	s_nop 1
	s_nop 1
	s_nop 1
	s_nop 1
	s_nop 1
	s_nop 1
	v_add_f32_e32 v93, 1.0, v118
	v_log_f32_e32 v93, v93
	s_nop 1
	v_mul_f32_e32 v93, 0x3f317218, v93
	s_nop 1
	s_nop 1
	s_nop 1
	v_add_f32_e32 v92, 1.0, v89
	v_log_f32_e32 v92, v92
	s_nop 1
	v_mul_f32_e32 v92, 0x3f317218, v92
	s_nop 1
	v_pk_add_f32 v[90:91], v[90:91], v[92:93] neg_lo:[0,1] neg_hi:[0,1]
	v_mul_f32_e64 v92, |v83|, s35
	v_exp_f32_e32 v121, v92
	v_min_f32_e32 v83, 0, v83
	v_pk_mul_f32 v[90:91], v[90:91], s[44:45] op_sel_hi:[1,0]
	s_nop 0
	s_nop 0
	s_nop 0
	s_nop 0
	s_nop 0
	s_nop 0
	s_nop 0
	s_nop 0
	s_nop 0
	s_nop 0
	s_nop 0
	s_nop 0
	s_nop 0
	s_nop 0
	s_nop 0
	s_nop 0
	s_nop 0
	s_nop 0
	s_nop 0
	v_mfma_f32_16x16x32_bf16 v[94:97], v[2:5], v[66:69], 0
	s_nop 1
	s_nop 1
	s_nop 1
	s_nop 1
	s_nop 1
	s_nop 1
	s_nop 1
	v_add_f32_e32 v93, 1.0, v121
	v_log_f32_e32 v93, v93
	s_nop 1
	v_mul_f32_e32 v93, 0x3f317218, v93
	s_nop 1
	s_nop 1
	s_nop 1
	v_add_f32_e32 v92, 1.0, v120
	v_log_f32_e32 v92, v92
	s_nop 1
	v_mul_f32_e32 v92, 0x3f317218, v92
	s_nop 1
	v_pk_add_f32 v[82:83], v[82:83], v[92:93] neg_lo:[0,1] neg_hi:[0,1]
	v_add_f32_e32 v89, v14, v94
	v_pk_mul_f32 v[92:93], v[82:83], s[44:45] op_sel_hi:[1,0]
	v_mul_f32_e64 v82, |v89|, s35
	v_exp_f32_e32 v120, v82
	v_lshl_add_u64 v[82:83], s[2:3], 2, v[70:71]
	global_store_dwordx4 v[82:83], v[90:93], off
	v_min_f32_e32 v82, 0, v89
	v_add_f32_e32 v83, v15, v95
	v_mul_f32_e64 v90, |v83|, s35
	v_exp_f32_e32 v121, v90
	v_min_f32_e32 v83, 0, v83
	s_nop 0
	s_nop 0
	s_nop 0
	s_nop 0
	s_nop 0
	s_nop 0
	s_nop 0
	s_nop 0
	s_nop 0
	s_nop 0
	s_nop 0
	s_nop 0
	s_nop 0
	s_nop 0
	s_nop 0
	s_nop 0
	s_nop 0
	s_nop 0
	s_nop 0
	s_nop 0
	v_add_f32_e32 v92, v16, v96
	s_nop 1
	s_nop 1
	s_nop 1
	s_nop 1
	s_nop 1
	s_nop 1
	s_nop 1
	v_add_f32_e32 v91, 1.0, v121
	v_log_f32_e32 v91, v91
	s_nop 1
	v_mul_f32_e32 v91, 0x3f317218, v91
	s_nop 1
	v_mul_f32_e64 v90, |v92|, s35
	v_exp_f32_e32 v121, v90
	s_nop 1
	s_nop 1
	v_add_f32_e32 v90, 1.0, v120
	v_log_f32_e32 v90, v90
	s_nop 1
	v_mul_f32_e32 v90, 0x3f317218, v90
	s_nop 1
	v_pk_add_f32 v[82:83], v[82:83], v[90:91] neg_lo:[0,1] neg_hi:[0,1]
	v_min_f32_e32 v90, 0, v92
	v_add_f32_e32 v91, v17, v97
	v_mul_f32_e64 v92, |v91|, s35
	v_exp_f32_e32 v120, v92
	v_min_f32_e32 v91, 0, v91
	s_nop 0
	s_nop 0
	s_nop 0
	s_nop 0
	s_nop 0
	s_nop 0
	s_nop 0
	s_nop 0
	s_nop 0
	s_nop 0
	s_nop 0
	s_nop 0
	s_nop 0
	s_nop 0
	s_nop 0
	s_nop 0
	s_nop 0
	s_nop 0
	s_nop 0
	s_nop 0
	v_mfma_f32_16x16x32_bf16 v[94:97], v[22:25], v[66:69], 0
	s_nop 1
	s_nop 1
	s_nop 1
	s_nop 1
	s_nop 1
	s_nop 1
	s_nop 1
	v_add_f32_e32 v93, 1.0, v120
	v_log_f32_e32 v93, v93
	s_nop 1
	v_mul_f32_e32 v93, 0x3f317218, v93
	s_nop 1
	s_nop 1
	s_nop 1
	v_add_f32_e32 v92, 1.0, v121
	v_log_f32_e32 v92, v92
	s_nop 1
	v_mul_f32_e32 v92, 0x3f317218, v92
	s_nop 1
	v_pk_add_f32 v[90:91], v[90:91], v[92:93] neg_lo:[0,1] neg_hi:[0,1]
	v_add_f32_e32 v89, v26, v94
	v_pk_mul_f32 v[92:93], v[90:91], s[44:45] op_sel_hi:[1,0]
	v_pk_mul_f32 v[90:91], v[82:83], s[44:45] op_sel_hi:[1,0]
	v_mul_f32_e64 v82, |v89|, s35
	v_exp_f32_e32 v120, v82
	v_lshl_add_u64 v[82:83], s[10:11], 2, v[70:71]
	global_store_dwordx4 v[82:83], v[90:93], off
	v_min_f32_e32 v82, 0, v89
	v_add_f32_e32 v83, v27, v95
	v_mul_f32_e64 v90, |v83|, s35
	v_exp_f32_e32 v121, v90
	v_min_f32_e32 v83, 0, v83
	s_nop 0
	s_nop 0
	s_nop 0
	s_nop 0
	s_nop 0
	s_nop 0
	s_nop 0
	s_nop 0
	s_nop 0
	s_nop 0
	s_nop 0
	s_nop 0
	s_nop 0
	s_nop 0
	s_nop 0
	s_nop 0
	s_nop 0
	s_nop 0
	s_nop 0
	s_nop 0
	v_add_f32_e32 v92, v28, v96
	s_nop 1
	s_nop 1
	s_nop 1
	s_nop 1
	s_nop 1
	s_nop 1
	s_nop 1
	v_add_f32_e32 v91, 1.0, v121
	v_log_f32_e32 v91, v91
	s_nop 1
	v_mul_f32_e32 v91, 0x3f317218, v91
	s_nop 1
	v_mul_f32_e64 v90, |v92|, s35
	v_exp_f32_e32 v121, v90
	s_nop 1
	s_nop 1
	v_add_f32_e32 v90, 1.0, v120
	v_log_f32_e32 v90, v90
	s_nop 1
	v_mul_f32_e32 v90, 0x3f317218, v90
	s_nop 1
	v_pk_add_f32 v[82:83], v[82:83], v[90:91] neg_lo:[0,1] neg_hi:[0,1]
	v_min_f32_e32 v90, 0, v92
	v_add_f32_e32 v91, v29, v97
	v_mul_f32_e64 v92, |v91|, s35
	v_exp_f32_e32 v120, v92
	v_min_f32_e32 v91, 0, v91
	s_nop 0
	s_nop 0
	s_nop 0
	s_nop 0
	s_nop 0
	s_nop 0
	s_nop 0
	s_nop 0
	s_nop 0
	s_nop 0
	s_nop 0
	s_nop 0
	s_nop 0
	s_nop 0
	s_nop 0
	s_nop 0
	s_nop 0
	s_nop 0
	s_nop 0
	s_nop 0
	v_mfma_f32_16x16x32_bf16 v[94:97], v[18:21], v[66:69], 0
	s_nop 1
	s_nop 1
	s_nop 1
	s_nop 1
	s_nop 1
	s_nop 1
	s_nop 1
	v_add_f32_e32 v93, 1.0, v120
	v_log_f32_e32 v93, v93
	s_nop 1
	v_mul_f32_e32 v93, 0x3f317218, v93
	s_nop 1
	s_nop 1
	s_nop 1
	v_add_f32_e32 v92, 1.0, v121
	v_log_f32_e32 v92, v92
	s_nop 1
	v_mul_f32_e32 v92, 0x3f317218, v92
	s_nop 1
	v_pk_add_f32 v[90:91], v[90:91], v[92:93] neg_lo:[0,1] neg_hi:[0,1]
	v_add_f32_e32 v89, v30, v94
	v_pk_mul_f32 v[92:93], v[90:91], s[44:45] op_sel_hi:[1,0]
	v_pk_mul_f32 v[90:91], v[82:83], s[44:45] op_sel_hi:[1,0]
	v_mul_f32_e64 v82, |v89|, s35
	v_exp_f32_e32 v120, v82
	v_lshl_add_u64 v[82:83], s[12:13], 2, v[70:71]
	global_store_dwordx4 v[82:83], v[90:93], off
	v_min_f32_e32 v82, 0, v89
	v_add_f32_e32 v83, v31, v95
	v_mul_f32_e64 v90, |v83|, s35
	v_exp_f32_e32 v121, v90
	v_min_f32_e32 v83, 0, v83
	s_nop 0
	s_nop 0
	s_nop 0
	s_nop 0
	s_nop 0
	s_nop 0
	s_nop 0
	s_nop 0
	s_nop 0
	s_nop 0
	s_nop 0
	s_nop 0
	s_nop 0
	s_nop 0
	s_nop 0
	s_nop 0
	s_nop 0
	s_nop 0
	s_nop 0
	s_nop 0
	v_add_f32_e32 v92, v32, v96
	s_nop 1
	s_nop 1
	s_nop 1
	s_nop 1
	s_nop 1
	s_nop 1
	s_nop 1
	v_add_f32_e32 v91, 1.0, v121
	v_log_f32_e32 v91, v91
	s_nop 1
	v_mul_f32_e32 v91, 0x3f317218, v91
	s_nop 1
	v_mul_f32_e64 v90, |v92|, s35
	v_exp_f32_e32 v121, v90
	s_nop 1
	s_nop 1
	v_add_f32_e32 v90, 1.0, v120
	v_log_f32_e32 v90, v90
	s_nop 1
	v_mul_f32_e32 v90, 0x3f317218, v90
	s_nop 1
	v_pk_add_f32 v[82:83], v[82:83], v[90:91] neg_lo:[0,1] neg_hi:[0,1]
	v_min_f32_e32 v90, 0, v92
	v_add_f32_e32 v91, v33, v97
	v_mul_f32_e64 v92, |v91|, s35
	v_exp_f32_e32 v120, v92
	v_min_f32_e32 v91, 0, v91
	s_nop 0
	s_nop 0
	s_nop 0
	s_nop 0
	s_nop 0
	s_nop 0
	s_nop 0
	s_nop 0
	s_nop 0
	s_nop 0
	s_nop 0
	s_nop 0
	s_nop 0
	s_nop 0
	s_nop 0
	s_nop 0
	s_nop 0
	s_nop 0
	s_nop 0
	s_nop 0
	v_mfma_f32_16x16x32_bf16 v[94:97], v[38:41], v[66:69], 0
	s_nop 1
	s_nop 1
	s_nop 1
	s_nop 1
	s_nop 1
	s_nop 1
	s_nop 1
	v_add_f32_e32 v93, 1.0, v120
	v_log_f32_e32 v93, v93
	s_nop 1
	v_mul_f32_e32 v93, 0x3f317218, v93
	s_nop 1
	s_nop 1
	s_nop 1
	v_add_f32_e32 v92, 1.0, v121
	v_log_f32_e32 v92, v92
	s_nop 1
	v_mul_f32_e32 v92, 0x3f317218, v92
	s_nop 1
	v_pk_add_f32 v[90:91], v[90:91], v[92:93] neg_lo:[0,1] neg_hi:[0,1]
	v_add_f32_e32 v89, v42, v94
	v_pk_mul_f32 v[92:93], v[90:91], s[44:45] op_sel_hi:[1,0]
	v_pk_mul_f32 v[90:91], v[82:83], s[44:45] op_sel_hi:[1,0]
	v_mul_f32_e64 v82, |v89|, s35
	v_exp_f32_e32 v120, v82
	v_lshl_add_u64 v[82:83], s[14:15], 2, v[70:71]
	global_store_dwordx4 v[82:83], v[90:93], off
	v_min_f32_e32 v82, 0, v89
	v_add_f32_e32 v83, v43, v95
	v_mul_f32_e64 v90, |v83|, s35
	v_exp_f32_e32 v121, v90
	v_min_f32_e32 v83, 0, v83
	s_nop 0
	s_nop 0
	s_nop 0
	s_nop 0
	s_nop 0
	s_nop 0
	s_nop 0
	s_nop 0
	s_nop 0
	s_nop 0
	s_nop 0
	s_nop 0
	s_nop 0
	s_nop 0
	s_nop 0
	s_nop 0
	s_nop 0
	s_nop 0
	s_nop 0
	s_nop 0
	v_add_f32_e32 v92, v44, v96
	s_nop 1
	s_nop 1
	s_nop 1
	s_nop 1
	s_nop 1
	s_nop 1
	s_nop 1
	v_add_f32_e32 v91, 1.0, v121
	v_log_f32_e32 v91, v91
	s_nop 1
	v_mul_f32_e32 v91, 0x3f317218, v91
	s_nop 1
	v_mul_f32_e64 v90, |v92|, s35
	v_exp_f32_e32 v121, v90
	s_nop 1
	s_nop 1
	v_add_f32_e32 v90, 1.0, v120
	v_log_f32_e32 v90, v90
	s_nop 1
	v_mul_f32_e32 v90, 0x3f317218, v90
	s_nop 1
	v_pk_add_f32 v[82:83], v[82:83], v[90:91] neg_lo:[0,1] neg_hi:[0,1]
	v_min_f32_e32 v90, 0, v92
	v_add_f32_e32 v91, v45, v97
	v_mul_f32_e64 v92, |v91|, s35
	v_exp_f32_e32 v120, v92
	v_min_f32_e32 v91, 0, v91
	s_nop 0
	s_nop 0
	s_nop 0
	s_nop 0
	s_nop 0
	s_nop 0
	s_nop 0
	s_nop 0
	s_nop 0
	s_nop 0
	s_nop 0
	s_nop 0
	s_nop 0
	s_nop 0
	s_nop 0
	s_nop 0
	s_nop 0
	s_nop 0
	s_nop 0
	s_nop 0
	v_mfma_f32_16x16x32_bf16 v[94:97], v[34:37], v[66:69], 0
	s_nop 1
	s_nop 1
	s_nop 1
	s_nop 1
	s_nop 1
	s_nop 1
	s_nop 1
	v_add_f32_e32 v93, 1.0, v120
	v_log_f32_e32 v93, v93
	s_nop 1
	v_mul_f32_e32 v93, 0x3f317218, v93
	s_nop 1
	s_nop 1
	s_nop 1
	v_add_f32_e32 v92, 1.0, v121
	v_log_f32_e32 v92, v92
	s_nop 1
	v_mul_f32_e32 v92, 0x3f317218, v92
	s_nop 1
	v_pk_add_f32 v[90:91], v[90:91], v[92:93] neg_lo:[0,1] neg_hi:[0,1]
	v_add_f32_e32 v89, v46, v94
	v_pk_mul_f32 v[92:93], v[90:91], s[44:45] op_sel_hi:[1,0]
	v_pk_mul_f32 v[90:91], v[82:83], s[44:45] op_sel_hi:[1,0]
	v_mul_f32_e64 v82, |v89|, s35
	v_exp_f32_e32 v120, v82
	v_lshl_add_u64 v[82:83], s[16:17], 2, v[70:71]
	global_store_dwordx4 v[82:83], v[90:93], off
	v_min_f32_e32 v82, 0, v89
	v_add_f32_e32 v83, v47, v95
	v_mul_f32_e64 v90, |v83|, s35
	v_exp_f32_e32 v121, v90
	v_min_f32_e32 v83, 0, v83
	s_nop 0
	s_nop 0
	s_nop 0
	s_nop 0
	s_nop 0
	s_nop 0
	s_nop 0
	s_nop 0
	s_nop 0
	s_nop 0
	s_nop 0
	s_nop 0
	s_nop 0
	s_nop 0
	s_nop 0
	s_nop 0
	s_nop 0
	s_nop 0
	s_nop 0
	s_nop 0
	v_add_f32_e32 v92, v48, v96
	s_nop 1
	s_nop 1
	s_nop 1
	s_nop 1
	s_nop 1
	s_nop 1
	s_nop 1
	v_add_f32_e32 v91, 1.0, v121
	v_log_f32_e32 v91, v91
	s_nop 1
	v_mul_f32_e32 v91, 0x3f317218, v91
	s_nop 1
	v_mul_f32_e64 v90, |v92|, s35
	v_exp_f32_e32 v121, v90
	s_nop 1
	s_nop 1
	v_add_f32_e32 v90, 1.0, v120
	v_log_f32_e32 v90, v90
	s_nop 1
	v_mul_f32_e32 v90, 0x3f317218, v90
	s_nop 1
	v_pk_add_f32 v[82:83], v[82:83], v[90:91] neg_lo:[0,1] neg_hi:[0,1]
	v_min_f32_e32 v90, 0, v92
	v_add_f32_e32 v91, v49, v97
	v_mul_f32_e64 v92, |v91|, s35
	v_exp_f32_e32 v120, v92
	v_min_f32_e32 v91, 0, v91
	s_nop 0
	s_nop 0
	s_nop 0
	s_nop 0
	s_nop 0
	s_nop 0
	s_nop 0
	s_nop 0
	s_nop 0
	s_nop 0
	s_nop 0
	s_nop 0
	s_nop 0
	s_nop 0
	s_nop 0
	s_nop 0
	s_nop 0
	s_nop 0
	s_nop 0
	s_nop 0
	v_mfma_f32_16x16x32_bf16 v[94:97], v[54:57], v[66:69], 0
	v_mfma_f32_16x16x32_bf16 v[66:69], v[50:53], v[66:69], 0
	s_nop 0
	s_nop 1
	s_nop 0
	s_nop 3
	v_add_f32_e32 v66, v62, v66
	v_add_f32_e32 v67, v63, v67
	v_add_f32_e32 v68, v64, v68
	v_add_f32_e32 v69, v65, v69
	s_nop 1
	s_nop 1
	s_nop 1
	v_add_f32_e32 v93, 1.0, v120
	v_log_f32_e32 v93, v93
	s_nop 1
	v_mul_f32_e32 v93, 0x3f317218, v93
	s_nop 1
	s_nop 1
	s_nop 1
	v_add_f32_e32 v92, 1.0, v121
	v_log_f32_e32 v92, v92
	s_nop 1
	v_mul_f32_e32 v92, 0x3f317218, v92
	s_nop 1
	v_pk_add_f32 v[90:91], v[90:91], v[92:93] neg_lo:[0,1] neg_hi:[0,1]
	v_add_f32_e32 v89, v58, v94
	v_pk_mul_f32 v[92:93], v[90:91], s[44:45] op_sel_hi:[1,0]
	v_pk_mul_f32 v[90:91], v[82:83], s[44:45] op_sel_hi:[1,0]
	v_mul_f32_e64 v82, |v89|, s35
	v_exp_f32_e32 v120, v82
	v_lshl_add_u64 v[82:83], s[18:19], 2, v[70:71]
	global_store_dwordx4 v[82:83], v[90:93], off
	v_min_f32_e32 v82, 0, v89
	v_add_f32_e32 v83, v59, v95
	v_mul_f32_e64 v90, |v83|, s35
	v_exp_f32_e32 v121, v90
	v_min_f32_e32 v83, 0, v83
	s_nop 0
	s_nop 0
	s_nop 0
	s_nop 0
	s_nop 0
	s_nop 0
	s_nop 0
	s_nop 0
	s_nop 0
	s_nop 0
	s_nop 0
	s_nop 0
	s_nop 0
	s_nop 0
	s_nop 0
	s_nop 0
	s_nop 0
	s_nop 0
	s_nop 0
	s_nop 0
	v_add_f32_e32 v92, v60, v96
	s_nop 1
	s_nop 1
	s_nop 1
	s_nop 1
	s_nop 1
	s_nop 1
	s_nop 1
	v_add_f32_e32 v91, 1.0, v121
	v_log_f32_e32 v91, v91
	s_nop 1
	v_mul_f32_e32 v91, 0x3f317218, v91
	s_nop 1
	v_mul_f32_e64 v90, |v92|, s35
	v_exp_f32_e32 v121, v90
	s_nop 1
	s_nop 1
	v_add_f32_e32 v90, 1.0, v120
	v_log_f32_e32 v90, v90
	s_nop 1
	v_mul_f32_e32 v90, 0x3f317218, v90
	s_nop 1
	v_pk_add_f32 v[82:83], v[82:83], v[90:91] neg_lo:[0,1] neg_hi:[0,1]
	v_min_f32_e32 v90, 0, v92
	v_add_f32_e32 v91, v61, v97
	v_mul_f32_e64 v92, |v91|, s35
	v_exp_f32_e32 v120, v92
	v_min_f32_e32 v91, 0, v91
	s_nop 0
	s_nop 0
	s_nop 0
	s_nop 0
	s_nop 0
	s_nop 0
	s_nop 0
	s_nop 0
	s_nop 0
	s_nop 0
	s_nop 0
	s_nop 0
	s_nop 0
	s_nop 0
	s_nop 0
	s_nop 0
	s_nop 0
	s_nop 0
	s_nop 0
	s_nop 0
	s_nop 0
	s_nop 1
	s_nop 1
	s_nop 1
	s_nop 1
	s_nop 1
	s_nop 1
	s_nop 1
	v_add_f32_e32 v93, 1.0, v120
	v_log_f32_e32 v93, v93
	s_nop 1
	v_mul_f32_e32 v93, 0x3f317218, v93
	s_nop 1
	s_nop 1
	s_nop 1
	v_add_f32_e32 v92, 1.0, v121
	v_log_f32_e32 v92, v92
	s_nop 1
	v_mul_f32_e32 v92, 0x3f317218, v92
	s_nop 1
	v_pk_add_f32 v[90:91], v[90:91], v[92:93] neg_lo:[0,1] neg_hi:[0,1]
	s_nop 0
	v_pk_mul_f32 v[92:93], v[90:91], s[44:45] op_sel_hi:[1,0]
	v_pk_mul_f32 v[90:91], v[82:83], s[44:45] op_sel_hi:[1,0]
	v_mul_f32_e64 v82, |v66|, s35
	v_exp_f32_e32 v89, v82
	v_lshl_add_u64 v[82:83], s[20:21], 2, v[70:71]
	global_store_dwordx4 v[82:83], v[90:93], off
	v_min_f32_e32 v66, 0, v66
	v_lshl_add_u64 v[70:71], s[22:23], 2, v[70:71]
	v_mul_f32_e64 v82, |v67|, s35
	v_exp_f32_e32 v116, v82
	v_min_f32_e32 v67, 0, v67
	s_nop 0
	s_nop 1
	s_nop 0
	s_nop 0
	s_nop 0
	s_nop 0
	s_nop 0
	s_nop 0
	s_nop 0
	s_nop 0
	s_nop 0
	s_nop 0
	s_nop 0
	s_nop 0
	s_nop 0
	s_nop 0
	s_nop 0
	s_nop 0
	s_nop 0
	v_mul_f32_e64 v90, |v68|, s35
	v_min_f32_e32 v68, 0, v68
	s_nop 0
	s_nop 1
	s_nop 1
	s_nop 1
	s_nop 1
	s_nop 1
	s_nop 1
	v_add_f32_e32 v83, 1.0, v116
	v_log_f32_e32 v83, v83
	s_nop 1
	v_mul_f32_e32 v83, 0x3f317218, v83
	s_nop 1
	v_exp_f32_e32 v116, v90
	s_nop 1
	s_nop 1
	v_add_f32_e32 v82, 1.0, v89
	v_log_f32_e32 v82, v82
	s_nop 1
	v_mul_f32_e32 v82, 0x3f317218, v82
	s_nop 1
	v_pk_add_f32 v[66:67], v[66:67], v[82:83] neg_lo:[0,1] neg_hi:[0,1]
	v_mul_f32_e64 v82, |v69|, s35
	v_exp_f32_e32 v117, v82
	v_min_f32_e32 v69, 0, v69
	v_pk_mul_f32 v[66:67], v[66:67], s[44:45] op_sel_hi:[1,0]
	s_nop 0
	s_nop 0
	s_nop 0
	s_nop 0
	s_nop 0
	s_nop 0
	s_nop 0
	s_nop 0
	s_nop 0
	s_nop 0
	s_nop 0
	s_nop 0
	s_nop 0
	s_nop 0
	s_nop 0
	s_nop 0
	s_nop 0
	s_nop 0
	s_nop 0
	s_nop 0
	s_nop 0
	s_nop 1
	s_nop 1
	s_nop 1
	s_nop 1
	s_nop 1
	s_nop 1
	s_nop 1
	v_add_f32_e32 v81, 1.0, v117
	v_log_f32_e32 v81, v81
	s_nop 1
	v_mul_f32_e32 v81, 0x3f317218, v81
	s_nop 1
	s_nop 1
	s_nop 1
	v_add_f32_e32 v80, 1.0, v116
	v_log_f32_e32 v80, v80
	s_nop 1
	v_mul_f32_e32 v80, 0x3f317218, v80
	s_nop 1
	v_pk_add_f32 v[68:69], v[68:69], v[80:81] neg_lo:[0,1] neg_hi:[0,1]
	s_nop 0
	v_pk_mul_f32 v[68:69], v[68:69], s[44:45] op_sel_hi:[1,0]
	global_store_dwordx4 v[70:71], v[66:69], off
	v_mov_b32_e32 v70, 0
	v_mov_b32_e32 v71, 0
	v_mov_b32_e32 v66, 0
	v_mov_b32_e32 v68, 0
	v_mov_b32_e32 v69, 0
	s_and_saveexec_b64 s[72:73], s[4:5]
	ds_read_b128 v[68:71], v72 offset:1024
	s_or_b64 exec, exec, s[72:73]
	s_waitcnt lgkmcnt(0)
	v_mfma_f32_16x16x32_bf16 v[90:93], v[6:9], v[68:71], 0
	v_lshl_add_u64 v[80:81], v[78:79], 0, s[64:65]
	s_nop 6
	v_add_f32_e32 v67, v10, v90
	v_mul_f32_e64 v82, |v67|, s35
	v_exp_f32_e32 v89, v82
	v_add_f32_e32 v91, v11, v91
	v_min_f32_e32 v90, 0, v67
	v_mul_f32_e64 v67, |v91|, s35
	v_exp_f32_e32 v67, v67
	v_min_f32_e32 v91, 0, v91
	v_add_f32_e32 v93, v13, v93
	s_nop 0
	s_nop 0
	s_nop 0
	s_nop 0
	s_nop 0
	s_nop 0
	s_nop 0
	s_nop 0
	s_nop 0
	s_nop 0
	s_nop 0
	s_nop 0
	s_nop 0
	s_nop 0
	s_nop 0
	s_nop 0
	s_nop 0
	s_nop 0
	s_nop 0
	s_nop 0
	s_nop 1
	s_nop 1
	s_nop 1
	s_nop 1
	s_nop 1
	s_nop 1
	s_nop 1
	v_add_f32_e32 v95, 1.0, v67
	v_log_f32_e32 v95, v95
	s_nop 1
	v_mul_f32_e32 v95, 0x3f317218, v95
	s_nop 1
	v_add_f32_e32 v67, v12, v92
	v_mul_f32_e64 v92, |v67|, s35
	v_exp_f32_e32 v122, v92
	v_min_f32_e32 v92, 0, v67
	s_nop 1
	v_add_f32_e32 v94, 1.0, v89
	v_log_f32_e32 v94, v94
	s_nop 1
	v_mul_f32_e32 v94, 0x3f317218, v94
	s_nop 1
	v_pk_add_f32 v[90:91], v[90:91], v[94:95] neg_lo:[0,1] neg_hi:[0,1]
	v_mul_f32_e64 v94, |v93|, s35
	v_exp_f32_e32 v123, v94
	v_min_f32_e32 v93, 0, v93
	v_pk_mul_f32 v[90:91], v[90:91], s[44:45] op_sel_hi:[1,0]
	s_nop 0
	s_nop 0
	s_nop 0
	s_nop 0
	s_nop 0
	s_nop 0
	s_nop 0
	s_nop 0
	s_nop 0
	s_nop 0
	s_nop 0
	s_nop 0
	s_nop 0
	s_nop 0
	s_nop 0
	s_nop 0
	s_nop 0
	s_nop 0
	v_lshl_add_u64 v[98:99], s[2:3], 2, v[80:81]
	s_nop 0
	s_nop 1
	s_nop 1
	s_nop 1
	s_nop 1
	s_nop 1
	s_nop 1
	s_nop 1
	v_add_f32_e32 v95, 1.0, v123
	v_log_f32_e32 v95, v95
	s_nop 1
	v_mul_f32_e32 v95, 0x3f317218, v95
	s_nop 1
	s_nop 1
	s_nop 1
	v_add_f32_e32 v94, 1.0, v122
	v_log_f32_e32 v94, v94
	s_nop 1
	v_mul_f32_e32 v94, 0x3f317218, v94
	s_nop 1
	v_pk_add_f32 v[92:93], v[92:93], v[94:95] neg_lo:[0,1] neg_hi:[0,1]
	v_mfma_f32_16x16x32_bf16 v[94:97], v[2:5], v[68:71], 0
	v_mul_f32_e64 v92, v92, s44
	v_mul_f32_e64 v93, v93, s44
	global_store_dwordx4 v[98:99], v[90:93], off
	s_nop 4
	v_add_f32_e32 v67, v14, v94
	v_mul_f32_e64 v89, |v67|, s35
	v_exp_f32_e32 v89, v89
	v_min_f32_e32 v90, 0, v67
	v_add_f32_e32 v91, v15, v95
	v_mul_f32_e64 v92, |v91|, s35
	v_exp_f32_e32 v122, v92
	v_min_f32_e32 v91, 0, v91
	s_nop 0
	s_nop 0
	s_nop 0
	s_nop 0
	s_nop 0
	s_nop 0
	s_nop 0
	s_nop 0
	s_nop 0
	s_nop 0
	s_nop 0
	s_nop 0
	s_nop 0
	s_nop 0
	s_nop 0
	s_nop 0
	s_nop 0
	s_nop 0
	s_nop 0
	s_nop 0
	v_add_f32_e32 v94, v16, v96
	s_nop 1
	s_nop 1
	s_nop 1
	s_nop 1
	s_nop 1
	s_nop 1
	s_nop 1
	v_add_f32_e32 v93, 1.0, v122
	v_log_f32_e32 v93, v93
	s_nop 1
	v_mul_f32_e32 v93, 0x3f317218, v93
	s_nop 1
	v_mul_f32_e64 v92, |v94|, s35
	v_exp_f32_e32 v122, v92
	s_nop 1
	s_nop 1
	v_add_f32_e32 v92, 1.0, v89
	v_log_f32_e32 v92, v92
	s_nop 1
	v_mul_f32_e32 v92, 0x3f317218, v92
	s_nop 1
	v_pk_add_f32 v[90:91], v[90:91], v[92:93] neg_lo:[0,1] neg_hi:[0,1]
	v_add_f32_e32 v93, v17, v97
	v_min_f32_e32 v92, 0, v94
	v_mul_f32_e64 v94, |v93|, s35
	v_exp_f32_e32 v123, v94
	v_min_f32_e32 v93, 0, v93
	v_pk_mul_f32 v[90:91], v[90:91], s[44:45] op_sel_hi:[1,0]
	s_nop 0
	s_nop 0
	s_nop 0
	s_nop 0
	s_nop 0
	s_nop 0
	s_nop 0
	s_nop 0
	s_nop 0
	s_nop 0
	s_nop 0
	s_nop 0
	s_nop 0
	s_nop 0
	s_nop 0
	s_nop 0
	s_nop 0
	s_nop 0
	v_lshl_add_u64 v[98:99], s[10:11], 2, v[80:81]
	s_nop 0
	s_nop 1
	s_nop 1
	s_nop 1
	s_nop 1
	s_nop 1
	s_nop 1
	s_nop 1
	v_add_f32_e32 v95, 1.0, v123
	v_log_f32_e32 v95, v95
	s_nop 1
	v_mul_f32_e32 v95, 0x3f317218, v95
	s_nop 1
	s_nop 1
	s_nop 1
	v_add_f32_e32 v94, 1.0, v122
	v_log_f32_e32 v94, v94
	s_nop 1
	v_mul_f32_e32 v94, 0x3f317218, v94
	s_nop 1
	v_pk_add_f32 v[92:93], v[92:93], v[94:95] neg_lo:[0,1] neg_hi:[0,1]
	v_mfma_f32_16x16x32_bf16 v[94:97], v[22:25], v[68:71], 0
	v_mul_f32_e64 v92, v92, s44
	v_mul_f32_e64 v93, v93, s44
	global_store_dwordx4 v[98:99], v[90:93], off
	s_nop 4
	v_add_f32_e32 v67, v26, v94
	v_mul_f32_e64 v89, |v67|, s35
	v_exp_f32_e32 v89, v89
	v_min_f32_e32 v90, 0, v67
	v_add_f32_e32 v91, v27, v95
	v_mul_f32_e64 v92, |v91|, s35
	v_exp_f32_e32 v122, v92
	v_min_f32_e32 v91, 0, v91
	s_nop 0
	s_nop 0
	s_nop 0
	s_nop 0
	s_nop 0
	s_nop 0
	s_nop 0
	s_nop 0
	s_nop 0
	s_nop 0
	s_nop 0
	s_nop 0
	s_nop 0
	s_nop 0
	s_nop 0
	s_nop 0
	s_nop 0
	s_nop 0
	s_nop 0
	s_nop 0
	v_add_f32_e32 v94, v28, v96
	s_nop 1
	s_nop 1
	s_nop 1
	s_nop 1
	s_nop 1
	s_nop 1
	s_nop 1
	v_add_f32_e32 v93, 1.0, v122
	v_log_f32_e32 v93, v93
	s_nop 1
	v_mul_f32_e32 v93, 0x3f317218, v93
	s_nop 1
	v_mul_f32_e64 v92, |v94|, s35
	v_exp_f32_e32 v122, v92
	s_nop 1
	s_nop 1
	v_add_f32_e32 v92, 1.0, v89
	v_log_f32_e32 v92, v92
	s_nop 1
	v_mul_f32_e32 v92, 0x3f317218, v92
	s_nop 1
	v_pk_add_f32 v[90:91], v[90:91], v[92:93] neg_lo:[0,1] neg_hi:[0,1]
	v_add_f32_e32 v93, v29, v97
	v_min_f32_e32 v92, 0, v94
	v_mul_f32_e64 v94, |v93|, s35
	v_exp_f32_e32 v123, v94
	v_min_f32_e32 v93, 0, v93
	v_pk_mul_f32 v[90:91], v[90:91], s[44:45] op_sel_hi:[1,0]
	s_nop 0
	s_nop 0
	s_nop 0
	s_nop 0
	s_nop 0
	s_nop 0
	s_nop 0
	s_nop 0
	s_nop 0
	s_nop 0
	s_nop 0
	s_nop 0
	s_nop 0
	s_nop 0
	s_nop 0
	s_nop 0
	s_nop 0
	s_nop 0
	v_lshl_add_u64 v[98:99], s[12:13], 2, v[80:81]
	s_nop 0
	s_nop 1
	s_nop 1
	s_nop 1
	s_nop 1
	s_nop 1
	s_nop 1
	s_nop 1
	v_add_f32_e32 v95, 1.0, v123
	v_log_f32_e32 v95, v95
	s_nop 1
	v_mul_f32_e32 v95, 0x3f317218, v95
	s_nop 1
	s_nop 1
	s_nop 1
	v_add_f32_e32 v94, 1.0, v122
	v_log_f32_e32 v94, v94
	s_nop 1
	v_mul_f32_e32 v94, 0x3f317218, v94
	s_nop 1
	v_pk_add_f32 v[92:93], v[92:93], v[94:95] neg_lo:[0,1] neg_hi:[0,1]
	v_mfma_f32_16x16x32_bf16 v[94:97], v[18:21], v[68:71], 0
	v_mul_f32_e64 v92, v92, s44
	v_mul_f32_e64 v93, v93, s44
	global_store_dwordx4 v[98:99], v[90:93], off
	s_nop 4
	v_add_f32_e32 v67, v30, v94
	v_mul_f32_e64 v89, |v67|, s35
	v_exp_f32_e32 v89, v89
	v_min_f32_e32 v90, 0, v67
	v_add_f32_e32 v91, v31, v95
	v_mul_f32_e64 v92, |v91|, s35
	v_exp_f32_e32 v122, v92
	v_min_f32_e32 v91, 0, v91
	s_nop 0
	s_nop 0
	s_nop 0
	s_nop 0
	s_nop 0
	s_nop 0
	s_nop 0
	s_nop 0
	s_nop 0
	s_nop 0
	s_nop 0
	s_nop 0
	s_nop 0
	s_nop 0
	s_nop 0
	s_nop 0
	s_nop 0
	s_nop 0
	s_nop 0
	s_nop 0
	v_add_f32_e32 v94, v32, v96
	s_nop 1
	s_nop 1
	s_nop 1
	s_nop 1
	s_nop 1
	s_nop 1
	s_nop 1
	v_add_f32_e32 v93, 1.0, v122
	v_log_f32_e32 v93, v93
	s_nop 1
	v_mul_f32_e32 v93, 0x3f317218, v93
	s_nop 1
	v_mul_f32_e64 v92, |v94|, s35
	v_exp_f32_e32 v122, v92
	s_nop 1
	s_nop 1
	v_add_f32_e32 v92, 1.0, v89
	v_log_f32_e32 v92, v92
	s_nop 1
	v_mul_f32_e32 v92, 0x3f317218, v92
	s_nop 1
	v_pk_add_f32 v[90:91], v[90:91], v[92:93] neg_lo:[0,1] neg_hi:[0,1]
	v_add_f32_e32 v93, v33, v97
	v_min_f32_e32 v92, 0, v94
	v_mul_f32_e64 v94, |v93|, s35
	v_exp_f32_e32 v123, v94
	v_min_f32_e32 v93, 0, v93
	v_pk_mul_f32 v[90:91], v[90:91], s[44:45] op_sel_hi:[1,0]
	s_nop 0
	s_nop 0
	s_nop 0
	s_nop 0
	s_nop 0
	s_nop 0
	s_nop 0
	s_nop 0
	s_nop 0
	s_nop 0
	s_nop 0
	s_nop 0
	s_nop 0
	s_nop 0
	s_nop 0
	s_nop 0
	s_nop 0
	s_nop 0
	v_lshl_add_u64 v[98:99], s[14:15], 2, v[80:81]
	s_nop 0
	s_nop 1
	s_nop 1
	s_nop 1
	s_nop 1
	s_nop 1
	s_nop 1
	s_nop 1
	v_add_f32_e32 v95, 1.0, v123
	v_log_f32_e32 v95, v95
	s_nop 1
	v_mul_f32_e32 v95, 0x3f317218, v95
	s_nop 1
	s_nop 1
	s_nop 1
	v_add_f32_e32 v94, 1.0, v122
	v_log_f32_e32 v94, v94
	s_nop 1
	v_mul_f32_e32 v94, 0x3f317218, v94
	s_nop 1
	v_pk_add_f32 v[92:93], v[92:93], v[94:95] neg_lo:[0,1] neg_hi:[0,1]
	v_mfma_f32_16x16x32_bf16 v[94:97], v[38:41], v[68:71], 0
	v_mul_f32_e64 v92, v92, s44
	v_mul_f32_e64 v93, v93, s44
	global_store_dwordx4 v[98:99], v[90:93], off
	s_nop 4
	v_add_f32_e32 v67, v42, v94
	v_mul_f32_e64 v89, |v67|, s35
	v_exp_f32_e32 v89, v89
	v_min_f32_e32 v90, 0, v67
	v_add_f32_e32 v91, v43, v95
	v_mul_f32_e64 v92, |v91|, s35
	v_exp_f32_e32 v122, v92
	v_min_f32_e32 v91, 0, v91
	s_nop 0
	s_nop 0
	s_nop 0
	s_nop 0
	s_nop 0
	s_nop 0
	s_nop 0
	s_nop 0
	s_nop 0
	s_nop 0
	s_nop 0
	s_nop 0
	s_nop 0
	s_nop 0
	s_nop 0
	s_nop 0
	s_nop 0
	s_nop 0
	s_nop 0
	s_nop 0
	v_add_f32_e32 v94, v44, v96
	s_nop 1
	s_nop 1
	s_nop 1
	s_nop 1
	s_nop 1
	s_nop 1
	s_nop 1
	v_add_f32_e32 v93, 1.0, v122
	v_log_f32_e32 v93, v93
	s_nop 1
	v_mul_f32_e32 v93, 0x3f317218, v93
	s_nop 1
	v_mul_f32_e64 v92, |v94|, s35
	v_exp_f32_e32 v122, v92
	s_nop 1
	s_nop 1
	v_add_f32_e32 v92, 1.0, v89
	v_log_f32_e32 v92, v92
	s_nop 1
	v_mul_f32_e32 v92, 0x3f317218, v92
	s_nop 1
	v_pk_add_f32 v[90:91], v[90:91], v[92:93] neg_lo:[0,1] neg_hi:[0,1]
	v_add_f32_e32 v93, v45, v97
	v_min_f32_e32 v92, 0, v94
	v_mul_f32_e64 v94, |v93|, s35
	v_exp_f32_e32 v123, v94
	v_min_f32_e32 v93, 0, v93
	v_pk_mul_f32 v[90:91], v[90:91], s[44:45] op_sel_hi:[1,0]
	s_nop 0
	s_nop 0
	s_nop 0
	s_nop 0
	s_nop 0
	s_nop 0
	s_nop 0
	s_nop 0
	s_nop 0
	s_nop 0
	s_nop 0
	s_nop 0
	s_nop 0
	s_nop 0
	s_nop 0
	s_nop 0
	s_nop 0
	s_nop 0
	v_lshl_add_u64 v[98:99], s[16:17], 2, v[80:81]
	s_nop 0
	s_nop 1
	s_nop 1
	s_nop 1
	s_nop 1
	s_nop 1
	s_nop 1
	s_nop 1
	v_add_f32_e32 v95, 1.0, v123
	v_log_f32_e32 v95, v95
	s_nop 1
	v_mul_f32_e32 v95, 0x3f317218, v95
	s_nop 1
	s_nop 1
	s_nop 1
	v_add_f32_e32 v94, 1.0, v122
	v_log_f32_e32 v94, v94
	s_nop 1
	v_mul_f32_e32 v94, 0x3f317218, v94
	s_nop 1
	v_pk_add_f32 v[92:93], v[92:93], v[94:95] neg_lo:[0,1] neg_hi:[0,1]
	v_mfma_f32_16x16x32_bf16 v[94:97], v[34:37], v[68:71], 0
	v_mul_f32_e64 v92, v92, s44
	v_mul_f32_e64 v93, v93, s44
	global_store_dwordx4 v[98:99], v[90:93], off
	s_nop 4
	v_add_f32_e32 v67, v46, v94
	v_mul_f32_e64 v89, |v67|, s35
	v_exp_f32_e32 v89, v89
	v_min_f32_e32 v90, 0, v67
	v_add_f32_e32 v91, v47, v95
	v_mul_f32_e64 v92, |v91|, s35
	v_exp_f32_e32 v122, v92
	v_min_f32_e32 v91, 0, v91
	s_nop 0
	s_nop 0
	s_nop 0
	s_nop 0
	s_nop 0
	s_nop 0
	s_nop 0
	s_nop 0
	s_nop 0
	s_nop 0
	s_nop 0
	s_nop 0
	s_nop 0
	s_nop 0
	s_nop 0
	s_nop 0
	s_nop 0
	s_nop 0
	s_nop 0
	s_nop 0
	v_add_f32_e32 v94, v48, v96
	s_nop 1
	s_nop 1
	s_nop 1
	s_nop 1
	s_nop 1
	s_nop 1
	s_nop 1
	v_add_f32_e32 v93, 1.0, v122
	v_log_f32_e32 v93, v93
	s_nop 1
	v_mul_f32_e32 v93, 0x3f317218, v93
	s_nop 1
	v_mul_f32_e64 v92, |v94|, s35
	v_exp_f32_e32 v122, v92
	s_nop 1
	s_nop 1
	v_add_f32_e32 v92, 1.0, v89
	v_log_f32_e32 v92, v92
	s_nop 1
	v_mul_f32_e32 v92, 0x3f317218, v92
	s_nop 1
	v_pk_add_f32 v[90:91], v[90:91], v[92:93] neg_lo:[0,1] neg_hi:[0,1]
	v_add_f32_e32 v93, v49, v97
	v_min_f32_e32 v92, 0, v94
	v_mul_f32_e64 v94, |v93|, s35
	v_exp_f32_e32 v123, v94
	v_min_f32_e32 v93, 0, v93
	v_pk_mul_f32 v[90:91], v[90:91], s[44:45] op_sel_hi:[1,0]
	s_nop 0
	s_nop 0
	s_nop 0
	s_nop 0
	s_nop 0
	s_nop 0
	s_nop 0
	s_nop 0
	s_nop 0
	s_nop 0
	s_nop 0
	s_nop 0
	s_nop 0
	s_nop 0
	s_nop 0
	s_nop 0
	s_nop 0
	s_nop 0
	v_lshl_add_u64 v[98:99], s[18:19], 2, v[80:81]
	s_nop 0
	s_nop 1
	s_nop 1
	s_nop 1
	s_nop 1
	s_nop 1
	s_nop 1
	s_nop 1
	v_add_f32_e32 v95, 1.0, v123
	v_log_f32_e32 v95, v95
	s_nop 1
	v_mul_f32_e32 v95, 0x3f317218, v95
	s_nop 1
	s_nop 1
	s_nop 1
	v_add_f32_e32 v94, 1.0, v122
	v_log_f32_e32 v94, v94
	s_nop 1
	v_mul_f32_e32 v94, 0x3f317218, v94
	s_nop 1
	v_pk_add_f32 v[92:93], v[92:93], v[94:95] neg_lo:[0,1] neg_hi:[0,1]
	v_mfma_f32_16x16x32_bf16 v[94:97], v[54:57], v[68:71], 0
	v_mul_f32_e64 v92, v92, s44
	v_mul_f32_e64 v93, v93, s44
	global_store_dwordx4 v[98:99], v[90:93], off
	v_mfma_f32_16x16x32_bf16 v[68:71], v[50:53], v[68:71], 0
	s_nop 3
	v_add_f32_e32 v67, v58, v94
	v_mul_f32_e64 v89, |v67|, s35
	v_exp_f32_e32 v89, v89
	v_min_f32_e32 v90, 0, v67
	v_add_f32_e32 v69, v63, v69
	v_add_f32_e32 v70, v64, v70
	v_add_f32_e32 v91, v59, v95
	v_mul_f32_e64 v92, |v91|, s35
	v_exp_f32_e32 v122, v92
	v_min_f32_e32 v91, 0, v91
	v_add_f32_e32 v71, v65, v71
	s_nop 0
	s_nop 0
	s_nop 0
	s_nop 0
	s_nop 0
	s_nop 0
	s_nop 0
	s_nop 0
	s_nop 0
	s_nop 0
	s_nop 0
	s_nop 0
	s_nop 0
	s_nop 0
	s_nop 0
	s_nop 0
	s_nop 0
	s_nop 0
	s_nop 0
	v_add_f32_e32 v94, v60, v96
	s_nop 1
	s_nop 1
	s_nop 1
	s_nop 1
	s_nop 1
	s_nop 1
	s_nop 1
	v_add_f32_e32 v93, 1.0, v122
	v_log_f32_e32 v93, v93
	s_nop 1
	v_mul_f32_e32 v93, 0x3f317218, v93
	s_nop 1
	v_mul_f32_e64 v92, |v94|, s35
	v_exp_f32_e32 v122, v92
	s_nop 1
	s_nop 1
	v_add_f32_e32 v92, 1.0, v89
	v_log_f32_e32 v92, v92
	s_nop 1
	v_mul_f32_e32 v92, 0x3f317218, v92
	s_nop 1
	v_pk_add_f32 v[90:91], v[90:91], v[92:93] neg_lo:[0,1] neg_hi:[0,1]
	v_add_f32_e32 v93, v61, v97
	v_min_f32_e32 v92, 0, v94
	v_mul_f32_e64 v94, |v93|, s35
	v_exp_f32_e32 v123, v94
	v_min_f32_e32 v93, 0, v93
	v_pk_mul_f32 v[90:91], v[90:91], s[44:45] op_sel_hi:[1,0]
	s_nop 0
	s_nop 0
	s_nop 0
	s_nop 0
	s_nop 0
	s_nop 0
	s_nop 0
	s_nop 0
	s_nop 0
	s_nop 0
	s_nop 0
	s_nop 0
	s_nop 0
	s_nop 0
	s_nop 0
	s_nop 0
	s_nop 0
	s_nop 0
	s_nop 0
	s_nop 0
	s_nop 1
	s_nop 1
	s_nop 1
	s_nop 1
	s_nop 1
	s_nop 1
	s_nop 1
	v_add_f32_e32 v95, 1.0, v123
	v_log_f32_e32 v95, v95
	s_nop 1
	v_mul_f32_e32 v95, 0x3f317218, v95
	s_nop 1
	s_nop 1
	s_nop 1
	v_add_f32_e32 v94, 1.0, v122
	v_log_f32_e32 v94, v94
	s_nop 1
	v_mul_f32_e32 v94, 0x3f317218, v94
	s_nop 1
	v_add_f32_e32 v67, v62, v68
	v_mul_f32_e64 v68, |v67|, s35
	v_exp_f32_e32 v89, v68
	v_pk_add_f32 v[92:93], v[92:93], v[94:95] neg_lo:[0,1] neg_hi:[0,1]
	v_lshl_add_u64 v[94:95], s[20:21], 2, v[80:81]
	v_pk_mul_f32 v[92:93], v[92:93], s[44:45] op_sel_hi:[1,0]
	v_min_f32_e32 v68, 0, v67
	global_store_dwordx4 v[94:95], v[90:93], off
	v_lshl_add_u64 v[80:81], s[22:23], 2, v[80:81]
	s_nop 0
	v_mul_f32_e64 v90, |v69|, s35
	v_exp_f32_e32 v118, v90
	v_min_f32_e32 v69, 0, v69
	s_nop 0
	s_nop 0
	s_nop 0
	s_nop 0
	s_nop 0
	s_nop 0
	s_nop 0
	s_nop 0
	s_nop 0
	s_nop 0
	s_nop 0
	s_nop 0
	s_nop 0
	s_nop 0
	s_nop 0
	s_nop 0
	s_nop 0
	s_nop 0
	s_nop 0
	s_nop 0
	s_nop 0
	s_nop 1
	s_nop 1
	s_nop 1
	s_nop 1
	s_nop 1
	s_nop 1
	s_nop 1
	v_add_f32_e32 v91, 1.0, v118
	v_log_f32_e32 v91, v91
	s_nop 1
	v_mul_f32_e32 v91, 0x3f317218, v91
	s_nop 1
	v_mul_f32_e64 v90, |v70|, s35
	v_exp_f32_e32 v118, v90
	v_min_f32_e32 v70, 0, v70
	s_nop 0
	s_nop 1
	v_add_f32_e32 v90, 1.0, v89
	v_log_f32_e32 v90, v90
	s_nop 1
	v_mul_f32_e32 v90, 0x3f317218, v90
	s_nop 1
	v_pk_add_f32 v[68:69], v[68:69], v[90:91] neg_lo:[0,1] neg_hi:[0,1]
	v_mul_f32_e64 v90, |v71|, s35
	v_exp_f32_e32 v119, v90
	v_min_f32_e32 v71, 0, v71
	v_pk_mul_f32 v[68:69], v[68:69], s[44:45] op_sel_hi:[1,0]
	s_nop 0
	s_nop 0
	s_nop 0
	s_nop 0
	s_nop 0
	s_nop 0
	s_nop 0
	s_nop 0
	s_nop 0
	s_nop 0
	s_nop 0
	s_nop 0
	s_nop 0
	s_nop 0
	s_nop 0
	s_nop 0
	s_nop 0
	s_nop 0
	s_nop 0
	s_nop 0
	s_nop 0
	s_nop 1
	s_nop 1
	s_nop 1
	s_nop 1
	s_nop 1
	s_nop 1
	s_nop 1
	v_add_f32_e32 v83, 1.0, v119
	v_log_f32_e32 v83, v83
	s_nop 1
	v_mul_f32_e32 v83, 0x3f317218, v83
	s_nop 1
	v_cmp_lt_f32_e64 vcc, |v118|, s45
	s_nop 1
	s_nop 1
	v_add_f32_e32 v82, 1.0, v118
	v_log_f32_e32 v82, v82
	s_nop 1
	v_mul_f32_e32 v82, 0x3f317218, v82
	s_nop 1
	v_pk_add_f32 v[70:71], v[70:71], v[82:83] neg_lo:[0,1] neg_hi:[0,1]
	v_mov_b32_e32 v67, 0
	v_pk_mul_f32 v[70:71], v[70:71], s[44:45] op_sel_hi:[1,0]
	global_store_dwordx4 v[80:81], v[68:71], off
	s_nop 1
	v_mov_b32_e32 v68, 0
	v_mov_b32_e32 v69, 0
	s_and_saveexec_b64 s[72:73], s[4:5]
	s_cbranch_execz .LBB0_146
	ds_read_b128 v[66:69], v72 offset:1536
	s_branch .LBB0_146
